# speedup vs baseline: 1.0089x; 1.0089x over previous
_Z11proj_kernelPKfPKDv8_DF16_PDF16_S4_S4_:
	v_mov_b32_e32 v164, 0x20000
	v_mov_b32_e32 v172, 0
	v_mov_b32_e32 v173, 0
	v_mov_b32_e32 v174, 0
	v_mov_b32_e32 v175, 0
	v_mov_b32_e32 v171, 0
	v_lshrrev_b32_e32 v169, 6, v0
	v_lshlrev_b32_e32 v169, 2, v169
	v_add_u32_e32 v169, 0x1fff0, v169
	ds_write_b128 v164, v[172:175]
	s_waitcnt lgkmcnt(0)
	s_barrier
	v_readfirstlane_b32 s13, v0
	s_lshl_b32 s12, s2, 6
	s_lshr_b32 s3, s2, 3
	s_cmpk_lt_u32 s13, 0x100
	v_and_b32_e32 v1, 15, v0
	s_mov_b64 s[4:5], -1
	s_cbranch_scc1 .LBB1_3
	s_andn2_b64 vcc, exec, s[4:5]
	s_cbranch_vccz .LBB1_4

.Lproj_poll_0:
	ds_read_b128 v[160:163], v164
	s_waitcnt lgkmcnt(0)
	v_min_u32_e32 v160, v160, v161
	v_min3_u32 v160, v160, v162, v163
	s_nop 0
	v_readfirstlane_b32 s20, v160
	s_nop 1
	s_cmp_ge_u32 s20, 1
	s_cbranch_scc1 .Lproj_go_0
	s_sleep 2
	s_branch .Lproj_poll_0
.Lproj_go_0:
	ds_read_b128 v[84:87], v57
	ds_read_b128 v[88:91], v57 offset:2048
	ds_read_b128 v[96:99], v57 offset:4096
	ds_read_b128 v[104:107], v57 offset:6144
	v_bfe_u32 v52, v0, 1, 3
	v_bitop3_b32 v52, v56, v52, 4 bitop3:0x36
	v_lshl_or_b32 v58, v52, 4, v54
	ds_read_b128 v[124:127], v58
	ds_read_b128 v[128:131], v58 offset:4096
	ds_read_b128 v[132:135], v58 offset:6144
	s_and_b32 s5, s5, 15
	s_mul_i32 s14, s5, 0x1800
	v_lshl_add_u64 v[52:53], v[18:19], 0, s[14:15]
	s_add_i32 s5, s3, 4
	s_and_b32 s5, s5, 15
	s_mul_i32 s14, s5, 0x1800
	s_add_i32 s5, s3, 5
	s_and_b32 s5, s5, 15
	s_xor_b32 s4, s4, 8
	v_or_b32_e32 v59, 0x1a000, v57
	s_ashr_i32 s13, s12, 31
	v_lshl_or_b32 v54, s16, 11, v54
	v_or_b32_e32 v156, s12, v1
	v_ashrrev_i32_e32 v157, 31, v156
	s_waitcnt vmcnt(17) lgkmcnt(6)
	v_mfma_f32_16x16x32_f16 v[92:95], v[84:87], v[2:5], 0
	s_waitcnt lgkmcnt(5)
	v_mfma_f32_16x16x32_f16 v[100:103], v[88:91], v[2:5], 0
	s_waitcnt lgkmcnt(4)
	v_mfma_f32_16x16x32_f16 v[108:111], v[96:99], v[2:5], 0
	s_waitcnt lgkmcnt(3)
	v_mfma_f32_16x16x32_f16 v[2:5], v[104:107], v[2:5], 0
	s_waitcnt vmcnt(16)
	v_mfma_f32_16x16x32_f16 v[112:115], v[6:9], v[84:87], 0
	s_waitcnt vmcnt(15)
	v_mfma_f32_16x16x32_f16 v[84:87], v[10:13], v[84:87], 0
	v_mfma_f32_16x16x32_f16 v[116:119], v[6:9], v[88:91], 0
	v_mfma_f32_16x16x32_f16 v[88:91], v[10:13], v[88:91], 0
	v_mfma_f32_16x16x32_f16 v[120:123], v[6:9], v[96:99], 0
	v_mfma_f32_16x16x32_f16 v[96:99], v[10:13], v[96:99], 0
	v_mfma_f32_16x16x32_f16 v[6:9], v[6:9], v[104:107], 0
	v_mfma_f32_16x16x32_f16 v[10:13], v[10:13], v[104:107], 0
	ds_read_b128 v[104:107], v58 offset:2048
	s_waitcnt vmcnt(12) lgkmcnt(3)
	v_mfma_f32_16x16x32_f16 v[92:95], v[124:127], v[24:27], v[92:95]
	s_waitcnt lgkmcnt(0)
	v_mfma_f32_16x16x32_f16 v[100:103], v[104:107], v[24:27], v[100:103]
	v_mfma_f32_16x16x32_f16 v[108:111], v[128:131], v[24:27], v[108:111]
	v_mfma_f32_16x16x32_f16 v[2:5], v[132:135], v[24:27], v[2:5]
	v_mfma_f32_16x16x32_f16 v[24:27], v[14:17], v[124:127], v[112:115]
	v_mfma_f32_16x16x32_f16 v[84:87], v[20:23], v[124:127], v[84:87]
	v_mfma_f32_16x16x32_f16 v[112:115], v[14:17], v[104:107], v[116:119]
	v_mfma_f32_16x16x32_f16 v[88:91], v[20:23], v[104:107], v[88:91]
	v_mfma_f32_16x16x32_f16 v[104:107], v[14:17], v[128:131], v[120:123]
	v_mfma_f32_16x16x32_f16 v[96:99], v[20:23], v[128:131], v[96:99]
	v_mfma_f32_16x16x32_f16 v[6:9], v[14:17], v[132:135], v[6:9]
	v_mfma_f32_16x16x32_f16 v[10:13], v[20:23], v[132:135], v[10:13]
	global_load_dwordx4 v[14:17], v[52:53], off
	global_load_dwordx4 v[20:23], v[52:53], off offset:1024
	global_load_dwordx4 v[116:119], v[52:53], off offset:2048
	global_load_dwordx4 v[120:123], v[52:53], off offset:3072
	v_add_co_u32_e32 v52, vcc, s2, v52
	s_nop 1
	v_addc_co_u32_e32 v53, vcc, 0, v53, vcc
	global_load_dwordx4 v[124:127], v[52:53], off
	global_load_dwordx4 v[128:131], v[52:53], off offset:1024
.Lproj_poll_1:
	ds_read_b128 v[160:163], v164
	s_waitcnt lgkmcnt(0)
	v_min_u32_e32 v160, v160, v161
	v_min3_u32 v160, v160, v162, v163
	s_nop 0
	v_readfirstlane_b32 s20, v160
	s_nop 1
	s_cmp_ge_u32 s20, 2
	s_cbranch_scc1 .Lproj_go_1
	s_sleep 2
	s_branch .Lproj_poll_1
.Lproj_go_1:
	ds_read_b128 v[132:135], v57 offset:8192
	ds_read_b128 v[136:139], v57 offset:10240
	s_waitcnt vmcnt(17) lgkmcnt(1)
	v_mfma_f32_16x16x32_f16 v[24:27], v[28:31], v[132:135], v[24:27]
	v_lshl_add_u64 v[52:53], v[18:19], 0, s[14:15]
	s_mul_i32 s14, s5, 0x1800
	s_add_i32 s5, s3, 6
	s_waitcnt vmcnt(16)
	v_mfma_f32_16x16x32_f16 v[84:87], v[32:35], v[132:135], v[84:87]
	s_and_b32 s5, s5, 15
	s_waitcnt vmcnt(15)
	v_mfma_f32_16x16x32_f16 v[92:95], v[132:135], v[36:39], v[92:95]
	s_waitcnt lgkmcnt(0)
	v_mfma_f32_16x16x32_f16 v[112:115], v[28:31], v[136:139], v[112:115]
	v_mfma_f32_16x16x32_f16 v[88:91], v[32:35], v[136:139], v[88:91]
	v_mfma_f32_16x16x32_f16 v[100:103], v[136:139], v[36:39], v[100:103]
	ds_read_b128 v[132:135], v57 offset:12288
	ds_read_b128 v[136:139], v57 offset:14336
	s_waitcnt lgkmcnt(1)
	v_mfma_f32_16x16x32_f16 v[104:107], v[28:31], v[132:135], v[104:107]
	v_mfma_f32_16x16x32_f16 v[96:99], v[32:35], v[132:135], v[96:99]
	s_waitcnt lgkmcnt(0)
	v_mfma_f32_16x16x32_f16 v[6:9], v[28:31], v[136:139], v[6:9]
	v_mfma_f32_16x16x32_f16 v[10:13], v[32:35], v[136:139], v[10:13]
	ds_read_b128 v[28:31], v58 offset:8192
	ds_read_b128 v[32:35], v58 offset:10240
	v_mfma_f32_16x16x32_f16 v[108:111], v[132:135], v[36:39], v[108:111]
	v_mfma_f32_16x16x32_f16 v[2:5], v[136:139], v[36:39], v[2:5]
	s_waitcnt vmcnt(14) lgkmcnt(1)
	v_mfma_f32_16x16x32_f16 v[24:27], v[40:43], v[28:31], v[24:27]
	s_waitcnt vmcnt(13)
	v_mfma_f32_16x16x32_f16 v[36:39], v[44:47], v[28:31], v[84:87]
	s_waitcnt vmcnt(12)
	v_mfma_f32_16x16x32_f16 v[28:31], v[28:31], v[48:51], v[92:95]
	s_waitcnt lgkmcnt(0)
	v_mfma_f32_16x16x32_f16 v[84:87], v[40:43], v[32:35], v[112:115]
	v_mfma_f32_16x16x32_f16 v[88:91], v[44:47], v[32:35], v[88:91]
	v_mfma_f32_16x16x32_f16 v[32:35], v[32:35], v[48:51], v[100:103]
	ds_read_b128 v[92:95], v58 offset:12288
	s_nop 1
	ds_read_b128 v[100:103], v58 offset:14336
	s_waitcnt lgkmcnt(1)
	v_mfma_f32_16x16x32_f16 v[104:107], v[40:43], v[92:95], v[104:107]
	v_mfma_f32_16x16x32_f16 v[96:99], v[44:47], v[92:95], v[96:99]
	v_mfma_f32_16x16x32_f16 v[92:95], v[92:95], v[48:51], v[108:111]
	s_waitcnt lgkmcnt(0)
	v_mfma_f32_16x16x32_f16 v[6:9], v[40:43], v[100:103], v[6:9]
	v_mfma_f32_16x16x32_f16 v[10:13], v[44:47], v[100:103], v[10:13]
	v_mfma_f32_16x16x32_f16 v[2:5], v[100:103], v[48:51], v[2:5]
	global_load_dwordx4 v[40:43], v[52:53], off
	global_load_dwordx4 v[44:47], v[52:53], off offset:1024
	global_load_dwordx4 v[48:51], v[52:53], off offset:2048
	global_load_dwordx4 v[100:103], v[52:53], off offset:3072
	v_add_co_u32_e32 v52, vcc, s2, v52
	s_nop 1
	v_addc_co_u32_e32 v53, vcc, 0, v53, vcc
	global_load_dwordx4 v[108:111], v[52:53], off
	global_load_dwordx4 v[112:115], v[52:53], off offset:1024
.Lproj_poll_2:
	ds_read_b128 v[160:163], v164
	s_waitcnt lgkmcnt(0)
	v_min_u32_e32 v160, v160, v161
	v_min3_u32 v160, v160, v162, v163
	s_nop 0
	v_readfirstlane_b32 s20, v160
	s_nop 1
	s_cmp_ge_u32 s20, 3
	s_cbranch_scc1 .Lproj_go_2
	s_sleep 2
	s_branch .Lproj_poll_2
.Lproj_go_2:
	ds_read_b128 v[132:135], v57 offset:16384
	ds_read_b128 v[136:139], v57 offset:18432
	s_waitcnt vmcnt(17) lgkmcnt(1)
	v_mfma_f32_16x16x32_f16 v[24:27], v[60:63], v[132:135], v[24:27]
	v_lshl_add_u64 v[52:53], v[18:19], 0, s[14:15]
	s_mul_i32 s14, s5, 0x1800
	s_add_i32 s5, s3, 7
	s_waitcnt vmcnt(16)
	v_mfma_f32_16x16x32_f16 v[36:39], v[64:67], v[132:135], v[36:39]
	s_and_b32 s5, s5, 15
	s_waitcnt vmcnt(15)
	v_mfma_f32_16x16x32_f16 v[28:31], v[132:135], v[68:71], v[28:31]
	s_waitcnt lgkmcnt(0)
	v_mfma_f32_16x16x32_f16 v[84:87], v[60:63], v[136:139], v[84:87]
	v_mfma_f32_16x16x32_f16 v[88:91], v[64:67], v[136:139], v[88:91]
	v_mfma_f32_16x16x32_f16 v[32:35], v[136:139], v[68:71], v[32:35]
	ds_read_b128 v[132:135], v57 offset:20480
	ds_read_b128 v[136:139], v57 offset:22528
	s_waitcnt lgkmcnt(1)
	v_mfma_f32_16x16x32_f16 v[104:107], v[60:63], v[132:135], v[104:107]
	v_mfma_f32_16x16x32_f16 v[96:99], v[64:67], v[132:135], v[96:99]
	s_waitcnt lgkmcnt(0)
	v_mfma_f32_16x16x32_f16 v[6:9], v[60:63], v[136:139], v[6:9]
	v_mfma_f32_16x16x32_f16 v[10:13], v[64:67], v[136:139], v[10:13]
	ds_read_b128 v[60:63], v58 offset:16384
	ds_read_b128 v[64:67], v58 offset:18432
	v_mfma_f32_16x16x32_f16 v[92:95], v[132:135], v[68:71], v[92:95]
	v_mfma_f32_16x16x32_f16 v[2:5], v[136:139], v[68:71], v[2:5]
	s_waitcnt vmcnt(14) lgkmcnt(1)
	v_mfma_f32_16x16x32_f16 v[24:27], v[72:75], v[60:63], v[24:27]
	s_waitcnt vmcnt(13)
	v_mfma_f32_16x16x32_f16 v[36:39], v[76:79], v[60:63], v[36:39]
	s_waitcnt vmcnt(12)
	v_mfma_f32_16x16x32_f16 v[28:31], v[60:63], v[80:83], v[28:31]
	s_waitcnt lgkmcnt(0)
	v_mfma_f32_16x16x32_f16 v[60:63], v[72:75], v[64:67], v[84:87]
	v_mfma_f32_16x16x32_f16 v[68:71], v[76:79], v[64:67], v[88:91]
	v_mfma_f32_16x16x32_f16 v[32:35], v[64:67], v[80:83], v[32:35]
	ds_read_b128 v[64:67], v58 offset:20480
	ds_read_b128 v[84:87], v58 offset:22528
	s_waitcnt lgkmcnt(1)
	v_mfma_f32_16x16x32_f16 v[88:91], v[72:75], v[64:67], v[104:107]
	v_mfma_f32_16x16x32_f16 v[96:99], v[76:79], v[64:67], v[96:99]
	v_mfma_f32_16x16x32_f16 v[64:67], v[64:67], v[80:83], v[92:95]
	s_waitcnt lgkmcnt(0)
	v_mfma_f32_16x16x32_f16 v[6:9], v[72:75], v[84:87], v[6:9]
	v_mfma_f32_16x16x32_f16 v[10:13], v[76:79], v[84:87], v[10:13]
	v_mfma_f32_16x16x32_f16 v[2:5], v[84:87], v[80:83], v[2:5]
	global_load_dwordx4 v[72:75], v[52:53], off
	global_load_dwordx4 v[76:79], v[52:53], off offset:1024
	global_load_dwordx4 v[80:83], v[52:53], off offset:2048
	global_load_dwordx4 v[84:87], v[52:53], off offset:3072
	v_add_co_u32_e32 v52, vcc, s2, v52
	s_nop 1
	v_addc_co_u32_e32 v53, vcc, 0, v53, vcc
	global_load_dwordx4 v[92:95], v[52:53], off
	global_load_dwordx4 v[104:107], v[52:53], off offset:1024
.Lproj_poll_3:
	ds_read_b128 v[160:163], v164
	s_waitcnt lgkmcnt(0)
	v_min_u32_e32 v160, v160, v161
	v_min3_u32 v160, v160, v162, v163
	s_nop 0
	v_readfirstlane_b32 s20, v160
	s_nop 1
	s_cmp_ge_u32 s20, 4
	s_cbranch_scc1 .Lproj_go_3
	s_sleep 2
	s_branch .Lproj_poll_3
.Lproj_go_3:
	ds_read_b128 v[132:135], v57 offset:24576
	ds_read_b128 v[136:139], v57 offset:26624
	s_waitcnt vmcnt(17) lgkmcnt(1)
	v_mfma_f32_16x16x32_f16 v[24:27], v[14:17], v[132:135], v[24:27]
	v_lshl_add_u64 v[52:53], v[18:19], 0, s[14:15]
	s_mul_i32 s14, s5, 0x1800
	s_waitcnt vmcnt(16)
	v_mfma_f32_16x16x32_f16 v[36:39], v[20:23], v[132:135], v[36:39]
	s_waitcnt vmcnt(15)
	v_mfma_f32_16x16x32_f16 v[28:31], v[132:135], v[116:119], v[28:31]
	s_waitcnt lgkmcnt(0)
	v_mfma_f32_16x16x32_f16 v[60:63], v[14:17], v[136:139], v[60:63]
	v_mfma_f32_16x16x32_f16 v[68:71], v[20:23], v[136:139], v[68:71]
	v_mfma_f32_16x16x32_f16 v[32:35], v[136:139], v[116:119], v[32:35]
	ds_read_b128 v[132:135], v57 offset:28672
	ds_read_b128 v[136:139], v57 offset:30720
	s_waitcnt lgkmcnt(1)
	v_mfma_f32_16x16x32_f16 v[88:91], v[14:17], v[132:135], v[88:91]
	v_mfma_f32_16x16x32_f16 v[96:99], v[20:23], v[132:135], v[96:99]
	s_waitcnt lgkmcnt(0)
	v_mfma_f32_16x16x32_f16 v[6:9], v[14:17], v[136:139], v[6:9]
	v_mfma_f32_16x16x32_f16 v[10:13], v[20:23], v[136:139], v[10:13]
	ds_read_b128 v[14:17], v58 offset:24576
	ds_read_b128 v[20:23], v58 offset:26624
	s_waitcnt vmcnt(14) lgkmcnt(1)
	v_mfma_f32_16x16x32_f16 v[24:27], v[120:123], v[14:17], v[24:27]
	s_waitcnt vmcnt(13)
	v_mfma_f32_16x16x32_f16 v[36:39], v[124:127], v[14:17], v[36:39]
	s_waitcnt vmcnt(12)
	v_mfma_f32_16x16x32_f16 v[14:17], v[14:17], v[128:131], v[28:31]
	s_waitcnt lgkmcnt(0)
	v_mfma_f32_16x16x32_f16 v[28:31], v[120:123], v[20:23], v[60:63]
	v_mfma_f32_16x16x32_f16 v[60:63], v[124:127], v[20:23], v[68:71]
	v_mfma_f32_16x16x32_f16 v[20:23], v[20:23], v[128:131], v[32:35]
	s_nop 2
	ds_read_b128 v[32:35], v58 offset:28672
	ds_read_b128 v[68:71], v58 offset:30720
	v_mfma_f32_16x16x32_f16 v[64:67], v[132:135], v[116:119], v[64:67]
	v_mfma_f32_16x16x32_f16 v[2:5], v[136:139], v[116:119], v[2:5]
	s_waitcnt lgkmcnt(1)
	v_mfma_f32_16x16x32_f16 v[88:91], v[120:123], v[32:35], v[88:91]
	v_mfma_f32_16x16x32_f16 v[96:99], v[124:127], v[32:35], v[96:99]
	v_mfma_f32_16x16x32_f16 v[32:35], v[32:35], v[128:131], v[64:67]
	s_waitcnt lgkmcnt(0)
	v_mfma_f32_16x16x32_f16 v[6:9], v[120:123], v[68:71], v[6:9]
	v_mfma_f32_16x16x32_f16 v[10:13], v[124:127], v[68:71], v[10:13]
	v_mfma_f32_16x16x32_f16 v[2:5], v[68:71], v[128:131], v[2:5]
	global_load_dwordx4 v[64:67], v[52:53], off
	global_load_dwordx4 v[68:71], v[52:53], off offset:1024
	global_load_dwordx4 v[116:119], v[52:53], off offset:2048
	global_load_dwordx4 v[120:123], v[52:53], off offset:3072
	v_add_co_u32_e32 v52, vcc, s2, v52
	s_nop 1
	v_addc_co_u32_e32 v53, vcc, 0, v53, vcc
	global_load_dwordx4 v[124:127], v[52:53], off
	global_load_dwordx4 v[128:131], v[52:53], off offset:1024
.Lproj_poll_4:
	ds_read_b128 v[160:163], v164
	s_waitcnt lgkmcnt(0)
	v_min_u32_e32 v160, v160, v161
	v_min3_u32 v160, v160, v162, v163
	s_nop 0
	v_readfirstlane_b32 s20, v160
	s_nop 1
	s_cmp_ge_u32 s20, 5
	s_cbranch_scc1 .Lproj_go_4
	s_sleep 2
	s_branch .Lproj_poll_4
.Lproj_go_4:
	ds_read_b128 v[132:135], v57 offset:32768
	ds_read_b128 v[136:139], v57 offset:34816
	s_waitcnt vmcnt(17) lgkmcnt(1)
	v_mfma_f32_16x16x32_f16 v[24:27], v[40:43], v[132:135], v[24:27]
	v_lshl_add_u64 v[52:53], v[18:19], 0, s[14:15]
	s_mul_i32 s14, s4, 0x1800
	s_add_i32 s4, s3, 9
	s_waitcnt vmcnt(16)
	v_mfma_f32_16x16x32_f16 v[36:39], v[44:47], v[132:135], v[36:39]
	s_and_b32 s4, s4, 15
	s_waitcnt vmcnt(15)
	v_mfma_f32_16x16x32_f16 v[14:17], v[132:135], v[48:51], v[14:17]
	s_waitcnt lgkmcnt(0)
	v_mfma_f32_16x16x32_f16 v[28:31], v[40:43], v[136:139], v[28:31]
	v_mfma_f32_16x16x32_f16 v[60:63], v[44:47], v[136:139], v[60:63]
	v_mfma_f32_16x16x32_f16 v[20:23], v[136:139], v[48:51], v[20:23]
	ds_read_b128 v[132:135], v57 offset:36864
	ds_read_b128 v[136:139], v57 offset:38912
	s_waitcnt lgkmcnt(1)
	v_mfma_f32_16x16x32_f16 v[88:91], v[40:43], v[132:135], v[88:91]
	v_mfma_f32_16x16x32_f16 v[96:99], v[44:47], v[132:135], v[96:99]
	s_waitcnt lgkmcnt(0)
	v_mfma_f32_16x16x32_f16 v[6:9], v[40:43], v[136:139], v[6:9]
	v_mfma_f32_16x16x32_f16 v[10:13], v[44:47], v[136:139], v[10:13]
	ds_read_b128 v[40:43], v58 offset:32768
	ds_read_b128 v[44:47], v58 offset:34816
	v_mfma_f32_16x16x32_f16 v[32:35], v[132:135], v[48:51], v[32:35]
	v_mfma_f32_16x16x32_f16 v[2:5], v[136:139], v[48:51], v[2:5]
	s_waitcnt vmcnt(14) lgkmcnt(1)
	v_mfma_f32_16x16x32_f16 v[24:27], v[100:103], v[40:43], v[24:27]
	s_waitcnt vmcnt(13)
	v_mfma_f32_16x16x32_f16 v[36:39], v[108:111], v[40:43], v[36:39]
	s_waitcnt vmcnt(12)
	v_mfma_f32_16x16x32_f16 v[14:17], v[40:43], v[112:115], v[14:17]
	s_waitcnt lgkmcnt(0)
	v_mfma_f32_16x16x32_f16 v[28:31], v[100:103], v[44:47], v[28:31]
	v_mfma_f32_16x16x32_f16 v[40:43], v[108:111], v[44:47], v[60:63]
	v_mfma_f32_16x16x32_f16 v[20:23], v[44:47], v[112:115], v[20:23]
	ds_read_b128 v[44:47], v58 offset:36864
	ds_read_b128 v[48:51], v58 offset:38912
	s_waitcnt lgkmcnt(1)
	v_mfma_f32_16x16x32_f16 v[60:63], v[100:103], v[44:47], v[88:91]
	v_mfma_f32_16x16x32_f16 v[88:91], v[108:111], v[44:47], v[96:99]
	v_mfma_f32_16x16x32_f16 v[32:35], v[44:47], v[112:115], v[32:35]
	s_waitcnt lgkmcnt(0)
	v_mfma_f32_16x16x32_f16 v[6:9], v[100:103], v[48:51], v[6:9]
	v_mfma_f32_16x16x32_f16 v[10:13], v[108:111], v[48:51], v[10:13]
	v_mfma_f32_16x16x32_f16 v[2:5], v[48:51], v[112:115], v[2:5]
	global_load_dwordx4 v[44:47], v[52:53], off
	global_load_dwordx4 v[48:51], v[52:53], off offset:1024
	global_load_dwordx4 v[96:99], v[52:53], off offset:2048
	global_load_dwordx4 v[100:103], v[52:53], off offset:3072
	v_add_co_u32_e32 v52, vcc, s2, v52
	s_nop 1
	v_addc_co_u32_e32 v53, vcc, 0, v53, vcc
	global_load_dwordx4 v[108:111], v[52:53], off
	global_load_dwordx4 v[112:115], v[52:53], off offset:1024
.Lproj_poll_5:
	ds_read_b128 v[160:163], v164
	s_waitcnt lgkmcnt(0)
	v_min_u32_e32 v160, v160, v161
	v_min3_u32 v160, v160, v162, v163
	s_nop 0
	v_readfirstlane_b32 s20, v160
	s_nop 1
	s_cmp_ge_u32 s20, 6
	s_cbranch_scc1 .Lproj_go_5
	s_sleep 2
	s_branch .Lproj_poll_5
.Lproj_go_5:
	ds_read_b128 v[132:135], v57 offset:40960
	ds_read_b128 v[136:139], v57 offset:43008
	s_waitcnt vmcnt(17) lgkmcnt(1)
	v_mfma_f32_16x16x32_f16 v[24:27], v[72:75], v[132:135], v[24:27]
	v_lshl_add_u64 v[52:53], v[18:19], 0, s[14:15]
	s_mul_i32 s14, s4, 0x1800
	s_add_i32 s4, s3, 10
	s_waitcnt vmcnt(16)
	v_mfma_f32_16x16x32_f16 v[36:39], v[76:79], v[132:135], v[36:39]
	s_and_b32 s4, s4, 15
	s_waitcnt vmcnt(15)
	v_mfma_f32_16x16x32_f16 v[14:17], v[132:135], v[80:83], v[14:17]
	s_waitcnt lgkmcnt(0)
	v_mfma_f32_16x16x32_f16 v[28:31], v[72:75], v[136:139], v[28:31]
	v_mfma_f32_16x16x32_f16 v[40:43], v[76:79], v[136:139], v[40:43]
	v_mfma_f32_16x16x32_f16 v[20:23], v[136:139], v[80:83], v[20:23]
	ds_read_b128 v[132:135], v57 offset:45056
	ds_read_b128 v[136:139], v57 offset:47104
	s_waitcnt lgkmcnt(1)
	v_mfma_f32_16x16x32_f16 v[60:63], v[72:75], v[132:135], v[60:63]
	v_mfma_f32_16x16x32_f16 v[88:91], v[76:79], v[132:135], v[88:91]
	s_waitcnt lgkmcnt(0)
	v_mfma_f32_16x16x32_f16 v[6:9], v[72:75], v[136:139], v[6:9]
	v_mfma_f32_16x16x32_f16 v[10:13], v[76:79], v[136:139], v[10:13]
	ds_read_b128 v[72:75], v58 offset:40960
	ds_read_b128 v[76:79], v58 offset:43008
	s_waitcnt vmcnt(14) lgkmcnt(1)
	v_mfma_f32_16x16x32_f16 v[24:27], v[84:87], v[72:75], v[24:27]
	s_waitcnt vmcnt(13)
	v_mfma_f32_16x16x32_f16 v[36:39], v[92:95], v[72:75], v[36:39]
	s_waitcnt vmcnt(12)
	v_mfma_f32_16x16x32_f16 v[14:17], v[72:75], v[104:107], v[14:17]
	s_waitcnt lgkmcnt(0)
	v_mfma_f32_16x16x32_f16 v[28:31], v[84:87], v[76:79], v[28:31]
	v_mfma_f32_16x16x32_f16 v[40:43], v[92:95], v[76:79], v[40:43]
	v_mfma_f32_16x16x32_f16 v[20:23], v[76:79], v[104:107], v[20:23]
	ds_read_b128 v[72:75], v58 offset:45056
	ds_read_b128 v[76:79], v58 offset:47104
	v_mfma_f32_16x16x32_f16 v[32:35], v[132:135], v[80:83], v[32:35]
	v_mfma_f32_16x16x32_f16 v[2:5], v[136:139], v[80:83], v[2:5]
	s_waitcnt lgkmcnt(1)
	v_mfma_f32_16x16x32_f16 v[60:63], v[84:87], v[72:75], v[60:63]
	v_mfma_f32_16x16x32_f16 v[80:83], v[92:95], v[72:75], v[88:91]
	v_mfma_f32_16x16x32_f16 v[32:35], v[72:75], v[104:107], v[32:35]
	s_waitcnt lgkmcnt(0)
	v_mfma_f32_16x16x32_f16 v[6:9], v[84:87], v[76:79], v[6:9]
	v_mfma_f32_16x16x32_f16 v[10:13], v[92:95], v[76:79], v[10:13]
	v_mfma_f32_16x16x32_f16 v[2:5], v[76:79], v[104:107], v[2:5]
	global_load_dwordx4 v[72:75], v[52:53], off
	global_load_dwordx4 v[76:79], v[52:53], off offset:1024
	global_load_dwordx4 v[84:87], v[52:53], off offset:2048
	global_load_dwordx4 v[88:91], v[52:53], off offset:3072
	v_add_co_u32_e32 v52, vcc, s2, v52
	s_nop 1
	v_addc_co_u32_e32 v53, vcc, 0, v53, vcc
	global_load_dwordx4 v[92:95], v[52:53], off
	global_load_dwordx4 v[104:107], v[52:53], off offset:1024
.Lproj_poll_6:
	ds_read_b128 v[160:163], v164
	s_waitcnt lgkmcnt(0)
	v_min_u32_e32 v160, v160, v161
	v_min3_u32 v160, v160, v162, v163
	s_nop 0
	v_readfirstlane_b32 s20, v160
	s_nop 1
	s_cmp_ge_u32 s20, 7
	s_cbranch_scc1 .Lproj_go_6
	s_sleep 2
	s_branch .Lproj_poll_6
.Lproj_go_6:
	ds_read_b128 v[132:135], v57 offset:49152
	ds_read_b128 v[136:139], v57 offset:51200
	s_waitcnt vmcnt(17) lgkmcnt(1)
	v_mfma_f32_16x16x32_f16 v[24:27], v[64:67], v[132:135], v[24:27]
	v_lshl_add_u64 v[52:53], v[18:19], 0, s[14:15]
	s_mul_i32 s14, s4, 0x1800
	s_add_i32 s4, s3, 11
	s_waitcnt vmcnt(16)
	v_mfma_f32_16x16x32_f16 v[36:39], v[68:71], v[132:135], v[36:39]
	s_and_b32 s4, s4, 15
	s_waitcnt vmcnt(15)
	v_mfma_f32_16x16x32_f16 v[14:17], v[132:135], v[116:119], v[14:17]
	s_waitcnt lgkmcnt(0)
	v_mfma_f32_16x16x32_f16 v[28:31], v[64:67], v[136:139], v[28:31]
	v_mfma_f32_16x16x32_f16 v[40:43], v[68:71], v[136:139], v[40:43]
	v_mfma_f32_16x16x32_f16 v[20:23], v[136:139], v[116:119], v[20:23]
	ds_read_b128 v[132:135], v57 offset:53248
	ds_read_b128 v[136:139], v57 offset:55296
	s_waitcnt lgkmcnt(1)
	v_mfma_f32_16x16x32_f16 v[60:63], v[64:67], v[132:135], v[60:63]
	v_mfma_f32_16x16x32_f16 v[80:83], v[68:71], v[132:135], v[80:83]
	s_waitcnt lgkmcnt(0)
	v_mfma_f32_16x16x32_f16 v[6:9], v[64:67], v[136:139], v[6:9]
	v_mfma_f32_16x16x32_f16 v[10:13], v[68:71], v[136:139], v[10:13]
	ds_read_b128 v[64:67], v58 offset:49152
	ds_read_b128 v[68:71], v58 offset:51200
	s_waitcnt vmcnt(14) lgkmcnt(1)
	v_mfma_f32_16x16x32_f16 v[24:27], v[120:123], v[64:67], v[24:27]
	s_waitcnt vmcnt(13)
	v_mfma_f32_16x16x32_f16 v[36:39], v[124:127], v[64:67], v[36:39]
	s_waitcnt vmcnt(12)
	v_mfma_f32_16x16x32_f16 v[14:17], v[64:67], v[128:131], v[14:17]
	s_waitcnt lgkmcnt(0)
	v_mfma_f32_16x16x32_f16 v[28:31], v[120:123], v[68:71], v[28:31]
	v_mfma_f32_16x16x32_f16 v[40:43], v[124:127], v[68:71], v[40:43]
	v_mfma_f32_16x16x32_f16 v[20:23], v[68:71], v[128:131], v[20:23]
	ds_read_b128 v[64:67], v58 offset:53248
	ds_read_b128 v[68:71], v58 offset:55296
	v_mfma_f32_16x16x32_f16 v[32:35], v[132:135], v[116:119], v[32:35]
	v_mfma_f32_16x16x32_f16 v[2:5], v[136:139], v[116:119], v[2:5]
	s_waitcnt lgkmcnt(1)
	v_mfma_f32_16x16x32_f16 v[60:63], v[120:123], v[64:67], v[60:63]
	v_mfma_f32_16x16x32_f16 v[80:83], v[124:127], v[64:67], v[80:83]
	v_mfma_f32_16x16x32_f16 v[32:35], v[64:67], v[128:131], v[32:35]
	s_waitcnt lgkmcnt(0)
	v_mfma_f32_16x16x32_f16 v[6:9], v[120:123], v[68:71], v[6:9]
	v_mfma_f32_16x16x32_f16 v[10:13], v[124:127], v[68:71], v[10:13]
	v_mfma_f32_16x16x32_f16 v[2:5], v[68:71], v[128:131], v[2:5]
	global_load_dwordx4 v[64:67], v[52:53], off
	global_load_dwordx4 v[68:71], v[52:53], off offset:1024
	global_load_dwordx4 v[116:119], v[52:53], off offset:2048
	global_load_dwordx4 v[120:123], v[52:53], off offset:3072
	v_add_co_u32_e32 v52, vcc, s2, v52
	s_nop 1
	v_addc_co_u32_e32 v53, vcc, 0, v53, vcc
	global_load_dwordx4 v[124:127], v[52:53], off
	global_load_dwordx4 v[128:131], v[52:53], off offset:1024
.Lproj_poll_7:
	ds_read_b128 v[160:163], v164
	s_waitcnt lgkmcnt(0)
	v_min_u32_e32 v160, v160, v161
	v_min3_u32 v160, v160, v162, v163
	s_nop 0
	v_readfirstlane_b32 s20, v160
	s_nop 1
	s_cmp_ge_u32 s20, 8
	s_cbranch_scc1 .Lproj_go_7
	s_sleep 2
	s_branch .Lproj_poll_7
.Lproj_go_7:
	ds_read_b128 v[132:135], v57 offset:57344
	ds_read_b128 v[136:139], v57 offset:59392
	s_waitcnt vmcnt(17) lgkmcnt(1)
	v_mfma_f32_16x16x32_f16 v[24:27], v[44:47], v[132:135], v[24:27]
	v_lshl_add_u64 v[52:53], v[18:19], 0, s[14:15]
	s_mul_i32 s14, s4, 0x1800
	s_add_i32 s4, s3, 12
	s_waitcnt vmcnt(16)
	v_mfma_f32_16x16x32_f16 v[36:39], v[48:51], v[132:135], v[36:39]
	s_and_b32 s4, s4, 15
	s_waitcnt vmcnt(15)
	v_mfma_f32_16x16x32_f16 v[14:17], v[132:135], v[96:99], v[14:17]
	s_waitcnt lgkmcnt(0)
	v_mfma_f32_16x16x32_f16 v[28:31], v[44:47], v[136:139], v[28:31]
	v_mfma_f32_16x16x32_f16 v[40:43], v[48:51], v[136:139], v[40:43]
	v_mfma_f32_16x16x32_f16 v[20:23], v[136:139], v[96:99], v[20:23]
	ds_read_b128 v[132:135], v57 offset:61440
	ds_read_b128 v[136:139], v57 offset:63488
	s_waitcnt lgkmcnt(1)
	v_mfma_f32_16x16x32_f16 v[60:63], v[44:47], v[132:135], v[60:63]
	v_mfma_f32_16x16x32_f16 v[80:83], v[48:51], v[132:135], v[80:83]
	s_waitcnt lgkmcnt(0)
	v_mfma_f32_16x16x32_f16 v[6:9], v[44:47], v[136:139], v[6:9]
	v_mfma_f32_16x16x32_f16 v[10:13], v[48:51], v[136:139], v[10:13]
	ds_read_b128 v[44:47], v58 offset:57344
	ds_read_b128 v[48:51], v58 offset:59392
	s_waitcnt vmcnt(14) lgkmcnt(1)
	v_mfma_f32_16x16x32_f16 v[24:27], v[100:103], v[44:47], v[24:27]
	s_waitcnt vmcnt(13)
	v_mfma_f32_16x16x32_f16 v[36:39], v[108:111], v[44:47], v[36:39]
	s_waitcnt vmcnt(12)
	v_mfma_f32_16x16x32_f16 v[14:17], v[44:47], v[112:115], v[14:17]
	s_waitcnt lgkmcnt(0)
	v_mfma_f32_16x16x32_f16 v[28:31], v[100:103], v[48:51], v[28:31]
	v_mfma_f32_16x16x32_f16 v[40:43], v[108:111], v[48:51], v[40:43]
	v_mfma_f32_16x16x32_f16 v[20:23], v[48:51], v[112:115], v[20:23]
	ds_read_b128 v[44:47], v58 offset:61440
	ds_read_b128 v[48:51], v58 offset:63488
	v_mfma_f32_16x16x32_f16 v[32:35], v[132:135], v[96:99], v[32:35]
	v_mfma_f32_16x16x32_f16 v[2:5], v[136:139], v[96:99], v[2:5]
	s_waitcnt lgkmcnt(1)
	v_mfma_f32_16x16x32_f16 v[60:63], v[100:103], v[44:47], v[60:63]
	v_mfma_f32_16x16x32_f16 v[80:83], v[108:111], v[44:47], v[80:83]
	v_mfma_f32_16x16x32_f16 v[32:35], v[44:47], v[112:115], v[32:35]
	s_waitcnt lgkmcnt(0)
	v_mfma_f32_16x16x32_f16 v[6:9], v[100:103], v[48:51], v[6:9]
	v_mfma_f32_16x16x32_f16 v[10:13], v[108:111], v[48:51], v[10:13]
	v_mfma_f32_16x16x32_f16 v[2:5], v[48:51], v[112:115], v[2:5]
	global_load_dwordx4 v[44:47], v[52:53], off
	global_load_dwordx4 v[48:51], v[52:53], off offset:1024
	global_load_dwordx4 v[96:99], v[52:53], off offset:2048
	global_load_dwordx4 v[100:103], v[52:53], off offset:3072
	v_add_co_u32_e32 v52, vcc, s2, v52
	s_nop 1
	v_addc_co_u32_e32 v53, vcc, 0, v53, vcc
	global_load_dwordx4 v[108:111], v[52:53], off
	global_load_dwordx4 v[112:115], v[52:53], off offset:1024
	v_or_b32_e32 v52, 0x10000, v57
.Lproj_poll_8:
	ds_read_b128 v[160:163], v164
	s_waitcnt lgkmcnt(0)
	v_min_u32_e32 v160, v160, v161
	v_min3_u32 v160, v160, v162, v163
	s_nop 0
	v_readfirstlane_b32 s20, v160
	s_nop 1
	s_cmp_ge_u32 s20, 9
	s_cbranch_scc1 .Lproj_go_8
	s_sleep 2
	s_branch .Lproj_poll_8
.Lproj_go_8:
	ds_read_b128 v[132:135], v52
	v_or_b32_e32 v52, 0x10800, v57
	ds_read_b128 v[136:139], v52
	v_or_b32_e32 v52, 0x11000, v57
	s_waitcnt vmcnt(17) lgkmcnt(1)
	v_mfma_f32_16x16x32_f16 v[24:27], v[72:75], v[132:135], v[24:27]
	s_waitcnt vmcnt(16)
	v_mfma_f32_16x16x32_f16 v[36:39], v[76:79], v[132:135], v[36:39]
	s_waitcnt vmcnt(15)
	v_mfma_f32_16x16x32_f16 v[14:17], v[132:135], v[84:87], v[14:17]
	ds_read_b128 v[132:135], v52
	v_or_b32_e32 v52, 0x11800, v57
	s_waitcnt lgkmcnt(1)
	v_mfma_f32_16x16x32_f16 v[28:31], v[72:75], v[136:139], v[28:31]
	v_mfma_f32_16x16x32_f16 v[40:43], v[76:79], v[136:139], v[40:43]
	v_mfma_f32_16x16x32_f16 v[20:23], v[136:139], v[84:87], v[20:23]
	ds_read_b128 v[136:139], v52
	v_or_b32_e32 v52, 0x10000, v58
	s_waitcnt lgkmcnt(1)
	v_mfma_f32_16x16x32_f16 v[60:63], v[72:75], v[132:135], v[60:63]
	s_waitcnt lgkmcnt(0)
	v_mfma_f32_16x16x32_f16 v[6:9], v[72:75], v[136:139], v[6:9]
	ds_read_b128 v[72:75], v52
	v_or_b32_e32 v52, 0x10800, v58
	v_mfma_f32_16x16x32_f16 v[80:83], v[76:79], v[132:135], v[80:83]
	v_mfma_f32_16x16x32_f16 v[10:13], v[76:79], v[136:139], v[10:13]
	ds_read_b128 v[76:79], v52
	v_or_b32_e32 v52, 0x11000, v58
	s_waitcnt vmcnt(14) lgkmcnt(1)
	v_mfma_f32_16x16x32_f16 v[24:27], v[88:91], v[72:75], v[24:27]
	s_waitcnt vmcnt(13)
	v_mfma_f32_16x16x32_f16 v[36:39], v[92:95], v[72:75], v[36:39]
	s_waitcnt vmcnt(12)
	v_mfma_f32_16x16x32_f16 v[14:17], v[72:75], v[104:107], v[14:17]
	ds_read_b128 v[72:75], v52
	v_or_b32_e32 v52, 0x11800, v58
	s_waitcnt lgkmcnt(1)
	v_mfma_f32_16x16x32_f16 v[28:31], v[88:91], v[76:79], v[28:31]
	v_mfma_f32_16x16x32_f16 v[40:43], v[92:95], v[76:79], v[40:43]
	v_mfma_f32_16x16x32_f16 v[20:23], v[76:79], v[104:107], v[20:23]
	ds_read_b128 v[76:79], v52
	v_lshl_add_u64 v[52:53], v[18:19], 0, s[14:15]
	s_mul_i32 s14, s4, 0x1800
	v_mfma_f32_16x16x32_f16 v[32:35], v[132:135], v[84:87], v[32:35]
	s_add_i32 s4, s3, 13
	s_and_b32 s4, s4, 15
	v_mfma_f32_16x16x32_f16 v[2:5], v[136:139], v[84:87], v[2:5]
	s_waitcnt lgkmcnt(1)
	v_mfma_f32_16x16x32_f16 v[60:63], v[88:91], v[72:75], v[60:63]
	v_mfma_f32_16x16x32_f16 v[80:83], v[92:95], v[72:75], v[80:83]
	v_mfma_f32_16x16x32_f16 v[32:35], v[72:75], v[104:107], v[32:35]
	s_waitcnt lgkmcnt(0)
	v_mfma_f32_16x16x32_f16 v[6:9], v[88:91], v[76:79], v[6:9]
	v_mfma_f32_16x16x32_f16 v[10:13], v[92:95], v[76:79], v[10:13]
	v_mfma_f32_16x16x32_f16 v[2:5], v[76:79], v[104:107], v[2:5]
	global_load_dwordx4 v[72:75], v[52:53], off
	global_load_dwordx4 v[76:79], v[52:53], off offset:1024
	global_load_dwordx4 v[84:87], v[52:53], off offset:2048
	global_load_dwordx4 v[88:91], v[52:53], off offset:3072
	v_add_co_u32_e32 v52, vcc, s2, v52
	s_nop 1
	v_addc_co_u32_e32 v53, vcc, 0, v53, vcc
	global_load_dwordx4 v[92:95], v[52:53], off
	global_load_dwordx4 v[104:107], v[52:53], off offset:1024
	v_or_b32_e32 v52, 0x12000, v57
.Lproj_poll_9:
	ds_read_b128 v[160:163], v164
	s_waitcnt lgkmcnt(0)
	v_min_u32_e32 v160, v160, v161
	v_min3_u32 v160, v160, v162, v163
	s_nop 0
	v_readfirstlane_b32 s20, v160
	s_nop 1
	s_cmp_ge_u32 s20, 10
	s_cbranch_scc1 .Lproj_go_9
	s_sleep 2
	s_branch .Lproj_poll_9
.Lproj_go_9:
	ds_read_b128 v[132:135], v52
	v_or_b32_e32 v52, 0x12800, v57
	ds_read_b128 v[136:139], v52
	v_or_b32_e32 v52, 0x13000, v57
	s_waitcnt vmcnt(17) lgkmcnt(1)
	v_mfma_f32_16x16x32_f16 v[24:27], v[64:67], v[132:135], v[24:27]
	s_waitcnt vmcnt(16)
	v_mfma_f32_16x16x32_f16 v[36:39], v[68:71], v[132:135], v[36:39]
	s_waitcnt vmcnt(15)
	v_mfma_f32_16x16x32_f16 v[14:17], v[132:135], v[116:119], v[14:17]
	ds_read_b128 v[132:135], v52
	v_or_b32_e32 v52, 0x13800, v57
	s_waitcnt lgkmcnt(1)
	v_mfma_f32_16x16x32_f16 v[28:31], v[64:67], v[136:139], v[28:31]
	v_mfma_f32_16x16x32_f16 v[40:43], v[68:71], v[136:139], v[40:43]
	v_mfma_f32_16x16x32_f16 v[20:23], v[136:139], v[116:119], v[20:23]
	ds_read_b128 v[136:139], v52
	v_or_b32_e32 v52, 0x12000, v58
	s_waitcnt lgkmcnt(1)
	v_mfma_f32_16x16x32_f16 v[60:63], v[64:67], v[132:135], v[60:63]
	s_waitcnt lgkmcnt(0)
	v_mfma_f32_16x16x32_f16 v[6:9], v[64:67], v[136:139], v[6:9]
	ds_read_b128 v[64:67], v52
	v_or_b32_e32 v52, 0x12800, v58
	v_mfma_f32_16x16x32_f16 v[80:83], v[68:71], v[132:135], v[80:83]
	v_mfma_f32_16x16x32_f16 v[10:13], v[68:71], v[136:139], v[10:13]
	ds_read_b128 v[68:71], v52
	v_or_b32_e32 v52, 0x13000, v58
	s_waitcnt vmcnt(14) lgkmcnt(1)
	v_mfma_f32_16x16x32_f16 v[24:27], v[120:123], v[64:67], v[24:27]
	s_waitcnt vmcnt(13)
	v_mfma_f32_16x16x32_f16 v[36:39], v[124:127], v[64:67], v[36:39]
	s_waitcnt vmcnt(12)
	v_mfma_f32_16x16x32_f16 v[14:17], v[64:67], v[128:131], v[14:17]
	ds_read_b128 v[64:67], v52
	v_or_b32_e32 v52, 0x13800, v58
	s_waitcnt lgkmcnt(1)
	v_mfma_f32_16x16x32_f16 v[28:31], v[120:123], v[68:71], v[28:31]
	v_mfma_f32_16x16x32_f16 v[40:43], v[124:127], v[68:71], v[40:43]
	v_mfma_f32_16x16x32_f16 v[20:23], v[68:71], v[128:131], v[20:23]
	ds_read_b128 v[68:71], v52
	v_lshl_add_u64 v[52:53], v[18:19], 0, s[14:15]
	s_mul_i32 s14, s4, 0x1800
	v_mfma_f32_16x16x32_f16 v[32:35], v[132:135], v[116:119], v[32:35]
	s_add_i32 s4, s3, 14
	s_and_b32 s4, s4, 15
	v_mfma_f32_16x16x32_f16 v[2:5], v[136:139], v[116:119], v[2:5]
	s_waitcnt lgkmcnt(1)
	v_mfma_f32_16x16x32_f16 v[60:63], v[120:123], v[64:67], v[60:63]
	v_mfma_f32_16x16x32_f16 v[80:83], v[124:127], v[64:67], v[80:83]
	v_mfma_f32_16x16x32_f16 v[32:35], v[64:67], v[128:131], v[32:35]
	s_waitcnt lgkmcnt(0)
	v_mfma_f32_16x16x32_f16 v[6:9], v[120:123], v[68:71], v[6:9]
	v_mfma_f32_16x16x32_f16 v[10:13], v[124:127], v[68:71], v[10:13]
	v_mfma_f32_16x16x32_f16 v[2:5], v[68:71], v[128:131], v[2:5]
	global_load_dwordx4 v[64:67], v[52:53], off
	global_load_dwordx4 v[68:71], v[52:53], off offset:1024
	global_load_dwordx4 v[116:119], v[52:53], off offset:2048
	global_load_dwordx4 v[120:123], v[52:53], off offset:3072
	v_add_co_u32_e32 v52, vcc, s2, v52
	s_nop 1
	v_addc_co_u32_e32 v53, vcc, 0, v53, vcc
	global_load_dwordx4 v[124:127], v[52:53], off
	global_load_dwordx4 v[128:131], v[52:53], off offset:1024
	v_or_b32_e32 v52, 0x14000, v57
.Lproj_poll_10:
	ds_read_b128 v[160:163], v164
	s_waitcnt lgkmcnt(0)
	v_min_u32_e32 v160, v160, v161
	v_min3_u32 v160, v160, v162, v163
	s_nop 0
	v_readfirstlane_b32 s20, v160
	s_nop 1
	s_cmp_ge_u32 s20, 11
	s_cbranch_scc1 .Lproj_go_10
	s_sleep 2
	s_branch .Lproj_poll_10
.Lproj_go_10:
	ds_read_b128 v[132:135], v52
	v_or_b32_e32 v52, 0x14800, v57
	ds_read_b128 v[136:139], v52
	v_or_b32_e32 v52, 0x15000, v57
	s_waitcnt vmcnt(17) lgkmcnt(1)
	v_mfma_f32_16x16x32_f16 v[24:27], v[44:47], v[132:135], v[24:27]
	s_waitcnt vmcnt(16)
	v_mfma_f32_16x16x32_f16 v[36:39], v[48:51], v[132:135], v[36:39]
	s_waitcnt vmcnt(15)
	v_mfma_f32_16x16x32_f16 v[14:17], v[132:135], v[96:99], v[14:17]
	ds_read_b128 v[132:135], v52
	v_or_b32_e32 v52, 0x15800, v57
	s_waitcnt lgkmcnt(1)
	v_mfma_f32_16x16x32_f16 v[28:31], v[44:47], v[136:139], v[28:31]
	v_mfma_f32_16x16x32_f16 v[40:43], v[48:51], v[136:139], v[40:43]
	v_mfma_f32_16x16x32_f16 v[20:23], v[136:139], v[96:99], v[20:23]
	ds_read_b128 v[136:139], v52
	s_waitcnt lgkmcnt(1)
	v_mfma_f32_16x16x32_f16 v[60:63], v[44:47], v[132:135], v[60:63]
	s_waitcnt lgkmcnt(0)
	v_mfma_f32_16x16x32_f16 v[6:9], v[44:47], v[136:139], v[6:9]
	v_or_b32_e32 v44, 0x14000, v58
	ds_read_b128 v[44:47], v44
	v_mfma_f32_16x16x32_f16 v[80:83], v[48:51], v[132:135], v[80:83]
	v_mfma_f32_16x16x32_f16 v[10:13], v[48:51], v[136:139], v[10:13]
	v_or_b32_e32 v48, 0x14800, v58
	ds_read_b128 v[48:51], v48
	s_waitcnt vmcnt(14) lgkmcnt(1)
	v_mfma_f32_16x16x32_f16 v[24:27], v[100:103], v[44:47], v[24:27]
	s_waitcnt vmcnt(13)
	v_mfma_f32_16x16x32_f16 v[36:39], v[108:111], v[44:47], v[36:39]
	s_waitcnt vmcnt(12)
	v_mfma_f32_16x16x32_f16 v[14:17], v[44:47], v[112:115], v[14:17]
	v_or_b32_e32 v44, 0x15000, v58
	ds_read_b128 v[44:47], v44
	s_waitcnt lgkmcnt(1)
	v_mfma_f32_16x16x32_f16 v[28:31], v[100:103], v[48:51], v[28:31]
	v_mfma_f32_16x16x32_f16 v[40:43], v[108:111], v[48:51], v[40:43]
	v_mfma_f32_16x16x32_f16 v[20:23], v[48:51], v[112:115], v[20:23]
	v_or_b32_e32 v48, 0x15800, v58
	ds_read_b128 v[48:51], v48
	v_mfma_f32_16x16x32_f16 v[32:35], v[132:135], v[96:99], v[32:35]
	v_mfma_f32_16x16x32_f16 v[2:5], v[136:139], v[96:99], v[2:5]
	s_waitcnt lgkmcnt(1)
	v_mfma_f32_16x16x32_f16 v[60:63], v[100:103], v[44:47], v[60:63]
	v_mfma_f32_16x16x32_f16 v[80:83], v[108:111], v[44:47], v[80:83]
	v_mfma_f32_16x16x32_f16 v[32:35], v[44:47], v[112:115], v[32:35]
	v_lshl_add_u64 v[44:45], v[18:19], 0, s[14:15]
	s_mul_i32 s14, s4, 0x1800
	s_add_i32 s4, s3, -1
	s_waitcnt lgkmcnt(0)
	v_mfma_f32_16x16x32_f16 v[6:9], v[100:103], v[48:51], v[6:9]
	s_and_b32 s4, s4, 15
	v_mfma_f32_16x16x32_f16 v[10:13], v[108:111], v[48:51], v[10:13]
	v_mfma_f32_16x16x32_f16 v[2:5], v[48:51], v[112:115], v[2:5]
	global_load_dwordx4 v[50:53], v[44:45], off
	global_load_dwordx4 v[96:99], v[44:45], off offset:1024
	global_load_dwordx4 v[100:103], v[44:45], off offset:2048
	global_load_dwordx4 v[108:111], v[44:45], off offset:3072
	v_add_co_u32_e32 v44, vcc, s2, v44
	v_or_b32_e32 v48, 0x16800, v57
	s_nop 0
	v_addc_co_u32_e32 v45, vcc, 0, v45, vcc
	global_load_dwordx4 v[112:115], v[44:45], off
	global_load_dwordx4 v[132:135], v[44:45], off offset:1024
	v_or_b32_e32 v44, 0x16000, v57
.Lproj_poll_11:
	ds_read_b128 v[160:163], v164
	s_waitcnt lgkmcnt(0)
	v_min_u32_e32 v160, v160, v161
	v_min3_u32 v160, v160, v162, v163
	s_nop 0
	v_readfirstlane_b32 s20, v160
	s_nop 1
	s_cmp_ge_u32 s20, 12
	s_cbranch_scc1 .Lproj_go_11
	s_sleep 2
	s_branch .Lproj_poll_11
.Lproj_go_11:
	ds_read_b128 v[44:47], v44
	ds_read_b128 v[136:139], v48
	s_waitcnt vmcnt(17) lgkmcnt(1)
	v_mfma_f32_16x16x32_f16 v[24:27], v[72:75], v[44:47], v[24:27]
	v_or_b32_e32 v48, 0x17800, v57
	s_waitcnt vmcnt(16)
	v_mfma_f32_16x16x32_f16 v[36:39], v[76:79], v[44:47], v[36:39]
	s_waitcnt vmcnt(15)
	v_mfma_f32_16x16x32_f16 v[14:17], v[44:47], v[84:87], v[14:17]
	v_or_b32_e32 v44, 0x17000, v57
	ds_read_b128 v[44:47], v44
	s_waitcnt lgkmcnt(1)
	v_mfma_f32_16x16x32_f16 v[28:31], v[72:75], v[136:139], v[28:31]
	v_mfma_f32_16x16x32_f16 v[40:43], v[76:79], v[136:139], v[40:43]
	v_mfma_f32_16x16x32_f16 v[20:23], v[136:139], v[84:87], v[20:23]
	ds_read_b128 v[136:139], v48
	v_or_b32_e32 v48, 0x16800, v58
	s_waitcnt lgkmcnt(1)
	v_mfma_f32_16x16x32_f16 v[60:63], v[72:75], v[44:47], v[60:63]
	v_mfma_f32_16x16x32_f16 v[80:83], v[76:79], v[44:47], v[80:83]
	v_mfma_f32_16x16x32_f16 v[32:35], v[44:47], v[84:87], v[32:35]
	v_or_b32_e32 v44, 0x16000, v58
	ds_read_b128 v[44:47], v44
	s_waitcnt lgkmcnt(1)
	v_mfma_f32_16x16x32_f16 v[6:9], v[72:75], v[136:139], v[6:9]
	ds_read_b128 v[72:75], v48
	v_mfma_f32_16x16x32_f16 v[10:13], v[76:79], v[136:139], v[10:13]
	v_mfma_f32_16x16x32_f16 v[2:5], v[136:139], v[84:87], v[2:5]
	s_waitcnt vmcnt(12) lgkmcnt(1)
	v_mfma_f32_16x16x32_f16 v[76:79], v[44:47], v[104:107], v[14:17]
	s_waitcnt lgkmcnt(0)
	v_mfma_f32_16x16x32_f16 v[84:87], v[92:95], v[72:75], v[40:43]
	s_nop 0
	v_or_b32_e32 v14, 0x17000, v58
	ds_read_b128 v[14:17], v14
	v_or_b32_e32 v40, 0x17800, v58
	ds_read_b128 v[40:43], v40
	v_mfma_f32_16x16x32_f16 v[24:27], v[88:91], v[44:47], v[24:27]
	v_mfma_f32_16x16x32_f16 v[36:39], v[92:95], v[44:47], v[36:39]
	v_mfma_f32_16x16x32_f16 v[28:31], v[88:91], v[72:75], v[28:31]
	v_mfma_f32_16x16x32_f16 v[20:23], v[72:75], v[104:107], v[20:23]
	s_waitcnt lgkmcnt(1)
	v_mfma_f32_16x16x32_f16 v[60:63], v[88:91], v[14:17], v[60:63]
	v_mfma_f32_16x16x32_f16 v[72:75], v[92:95], v[14:17], v[80:83]
	s_waitcnt lgkmcnt(0)
	v_mfma_f32_16x16x32_f16 v[80:83], v[88:91], v[40:43], v[6:9]
	v_mfma_f32_16x16x32_f16 v[88:91], v[92:95], v[40:43], v[10:13]
	v_mfma_f32_16x16x32_f16 v[92:95], v[40:43], v[104:107], v[2:5]
	v_or_b32_e32 v40, 0x18000, v57
	s_nop 1
	v_lshl_add_u64 v[2:3], v[18:19], 0, s[14:15]
	v_mfma_f32_16x16x32_f16 v[32:35], v[14:17], v[104:107], v[32:35]
	global_load_dwordx4 v[46:49], v[2:3], off
	global_load_dwordx4 v[42:45], v[2:3], off offset:1024
	global_load_dwordx4 v[14:17], v[2:3], off offset:2048
	global_load_dwordx4 v[10:13], v[2:3], off offset:3072
	v_add_co_u32_e32 v2, vcc, s2, v2
	s_mul_i32 s14, s4, 0x1800
	s_nop 0
	v_addc_co_u32_e32 v3, vcc, 0, v3, vcc
	global_load_dwordx4 v[6:9], v[2:3], off
	s_nop 0
	global_load_dwordx4 v[2:5], v[2:3], off offset:1024
.Lproj_poll_12:
	ds_read_b128 v[160:163], v164
	s_waitcnt lgkmcnt(0)
	v_min_u32_e32 v160, v160, v161
	v_min3_u32 v160, v160, v162, v163
	s_nop 0
	v_readfirstlane_b32 s20, v160
	s_nop 1
	s_cmp_ge_u32 s20, 13
	s_cbranch_scc1 .Lproj_go_12
	s_sleep 2
	s_branch .Lproj_poll_12
.Lproj_go_12:
	ds_read_b128 v[104:107], v40
	v_or_b32_e32 v40, 0x18800, v57
	ds_read_b128 v[136:139], v40
	v_or_b32_e32 v40, 0x19000, v57
	s_waitcnt vmcnt(17) lgkmcnt(1)
	v_mfma_f32_16x16x32_f16 v[24:27], v[64:67], v[104:107], v[24:27]
	v_lshl_add_u64 v[18:19], v[18:19], 0, s[14:15]
	s_lshl_b64 s[4:5], s[12:13], 7
	s_add_u32 s4, s10, s4
	s_waitcnt vmcnt(16)
	v_mfma_f32_16x16x32_f16 v[36:39], v[68:71], v[104:107], v[36:39]
	s_addc_u32 s5, s11, s5
	s_waitcnt vmcnt(15)
	v_mfma_f32_16x16x32_f16 v[76:79], v[104:107], v[116:119], v[76:79]
	ds_read_b128 v[104:107], v40
	v_or_b32_e32 v40, 0x19800, v57
	s_waitcnt lgkmcnt(1)
	v_mfma_f32_16x16x32_f16 v[28:31], v[64:67], v[136:139], v[28:31]
	v_mfma_f32_16x16x32_f16 v[84:87], v[68:71], v[136:139], v[84:87]
	v_mfma_f32_16x16x32_f16 v[20:23], v[136:139], v[116:119], v[20:23]
	ds_read_b128 v[136:139], v40
	v_or_b32_e32 v40, 0x18000, v58
	s_waitcnt lgkmcnt(1)
	v_mfma_f32_16x16x32_f16 v[72:75], v[68:71], v[104:107], v[72:75]
	s_waitcnt lgkmcnt(0)
	v_mfma_f32_16x16x32_f16 v[68:71], v[68:71], v[136:139], v[88:91]
	s_nop 2
	ds_read_b128 v[88:91], v40
	v_or_b32_e32 v40, 0x18800, v58
	v_mfma_f32_16x16x32_f16 v[60:63], v[64:67], v[104:107], v[60:63]
	v_mfma_f32_16x16x32_f16 v[64:67], v[64:67], v[136:139], v[80:83]
	v_mfma_f32_16x16x32_f16 v[80:83], v[136:139], v[116:119], v[92:95]
	s_nop 2
	ds_read_b128 v[92:95], v40
	v_mfma_f32_16x16x32_f16 v[32:35], v[104:107], v[116:119], v[32:35]
	s_waitcnt vmcnt(14) lgkmcnt(1)
	v_mfma_f32_16x16x32_f16 v[104:107], v[120:123], v[88:91], v[24:27]
	s_nop 2
	v_or_b32_e32 v24, 0x19000, v58
	s_waitcnt vmcnt(13)
	v_mfma_f32_16x16x32_f16 v[116:119], v[124:127], v[88:91], v[36:39]
	s_waitcnt vmcnt(12)
	v_mfma_f32_16x16x32_f16 v[76:79], v[88:91], v[128:131], v[76:79]
	s_waitcnt lgkmcnt(0)
	v_mfma_f32_16x16x32_f16 v[88:91], v[120:123], v[92:95], v[28:31]
	v_mfma_f32_16x16x32_f16 v[84:87], v[124:127], v[92:95], v[84:87]
	v_mfma_f32_16x16x32_f16 v[92:95], v[92:95], v[128:131], v[20:23]
	s_nop 2
	ds_read_b128 v[20:23], v24
	v_or_b32_e32 v24, 0x19800, v58
	ds_read_b128 v[24:27], v24
	s_waitcnt lgkmcnt(1)
	v_mfma_f32_16x16x32_f16 v[60:63], v[120:123], v[20:23], v[60:63]
	v_mfma_f32_16x16x32_f16 v[72:75], v[124:127], v[20:23], v[72:75]
	v_mfma_f32_16x16x32_f16 v[136:139], v[20:23], v[128:131], v[32:35]
	s_waitcnt lgkmcnt(0)
	v_mfma_f32_16x16x32_f16 v[64:67], v[120:123], v[24:27], v[64:67]
	v_mfma_f32_16x16x32_f16 v[68:71], v[124:127], v[24:27], v[68:71]
	v_mfma_f32_16x16x32_f16 v[80:83], v[24:27], v[128:131], v[80:83]
	global_load_dwordx4 v[38:41], v[18:19], off
	global_load_dwordx4 v[34:37], v[18:19], off offset:1024
	global_load_dwordx4 v[30:33], v[18:19], off offset:2048
	global_load_dwordx4 v[22:25], v[18:19], off offset:3072
	v_add_co_u32_e32 v18, vcc, s2, v18
	s_mov_b32 s2, 0x3c800000
	s_nop 0
	v_addc_co_u32_e32 v19, vcc, 0, v19, vcc
	global_load_dwordx4 v[26:29], v[18:19], off
	s_nop 0
	global_load_dwordx4 v[18:21], v[18:19], off offset:1024
.Lproj_poll_13:
	ds_read_b128 v[160:163], v164
	s_waitcnt lgkmcnt(0)
	v_min_u32_e32 v160, v160, v161
	v_min3_u32 v160, v160, v162, v163
	s_nop 0
	v_readfirstlane_b32 s20, v160
	s_nop 1
	s_cmp_ge_u32 s20, 14
	s_cbranch_scc1 .Lproj_go_13
	s_sleep 2
	s_branch .Lproj_poll_13
.Lproj_go_13:
	ds_read_b128 v[120:123], v59
	v_or_b32_e32 v59, 0x1a800, v57
	ds_read_b128 v[124:127], v59
	v_or_b32_e32 v59, 0x1b000, v57
	s_waitcnt vmcnt(17) lgkmcnt(1)
	v_mfma_f32_16x16x32_f16 v[104:107], v[50:53], v[120:123], v[104:107]
	s_waitcnt vmcnt(16)
	v_mfma_f32_16x16x32_f16 v[116:119], v[96:99], v[120:123], v[116:119]
	s_waitcnt vmcnt(15)
	v_mfma_f32_16x16x32_f16 v[76:79], v[120:123], v[100:103], v[76:79]
	ds_read_b128 v[120:123], v59
	v_or_b32_e32 v59, 0x1b800, v57
	s_waitcnt lgkmcnt(1)
	v_mfma_f32_16x16x32_f16 v[88:91], v[50:53], v[124:127], v[88:91]
	v_mfma_f32_16x16x32_f16 v[84:87], v[96:99], v[124:127], v[84:87]
	v_mfma_f32_16x16x32_f16 v[92:95], v[124:127], v[100:103], v[92:95]
	ds_read_b128 v[124:127], v59
	v_or_b32_e32 v59, 0x1a000, v58
	s_waitcnt lgkmcnt(1)
	v_mfma_f32_16x16x32_f16 v[60:63], v[50:53], v[120:123], v[60:63]
	s_waitcnt lgkmcnt(0)
	v_mfma_f32_16x16x32_f16 v[50:53], v[50:53], v[124:127], v[64:67]
	v_mfma_f32_16x16x32_f16 v[64:67], v[96:99], v[124:127], v[68:71]
	v_mfma_f32_16x16x32_f16 v[68:71], v[124:127], v[100:103], v[80:83]
	v_or_b32_e32 v124, 0x1d800, v58
	s_nop 1
	ds_read_b128 v[80:83], v59
	v_or_b32_e32 v59, 0x1a800, v58
	v_mfma_f32_16x16x32_f16 v[72:75], v[96:99], v[120:123], v[72:75]
	ds_read_b128 v[96:99], v59
	v_or_b32_e32 v59, 0x1b000, v58
	v_mfma_f32_16x16x32_f16 v[120:123], v[120:123], v[100:103], v[136:139]
	s_waitcnt vmcnt(14) lgkmcnt(1)
	v_mfma_f32_16x16x32_f16 v[100:103], v[108:111], v[80:83], v[104:107]
	s_waitcnt vmcnt(13)
	v_mfma_f32_16x16x32_f16 v[104:107], v[112:115], v[80:83], v[116:119]
	s_waitcnt vmcnt(12)
	v_mfma_f32_16x16x32_f16 v[76:79], v[80:83], v[132:135], v[76:79]
	s_waitcnt lgkmcnt(0)
	v_mfma_f32_16x16x32_f16 v[80:83], v[108:111], v[96:99], v[88:91]
	v_mfma_f32_16x16x32_f16 v[88:91], v[96:99], v[132:135], v[92:95]
	s_nop 2
	ds_read_b128 v[92:95], v59
	v_or_b32_e32 v59, 0x1b800, v58
	v_mfma_f32_16x16x32_f16 v[84:87], v[112:115], v[96:99], v[84:87]
	ds_read_b128 v[96:99], v59
	v_or_b32_e32 v59, 0x1c000, v57
	s_waitcnt lgkmcnt(0)
	v_mfma_f32_16x16x32_f16 v[60:63], v[108:111], v[92:95], v[60:63]
.Lproj_poll_14:
	ds_read_b128 v[160:163], v164
	s_waitcnt lgkmcnt(0)
	v_min_u32_e32 v160, v160, v161
	v_min3_u32 v160, v160, v162, v163
	s_nop 0
	v_readfirstlane_b32 s20, v160
	s_nop 1
	s_cmp_ge_u32 s20, 15
	s_cbranch_scc1 .Lproj_go_14
	s_sleep 2
	s_branch .Lproj_poll_14
.Lproj_go_14:
	v_mfma_f32_16x16x32_f16 v[108:111], v[108:111], v[96:99], v[50:53]
	v_mfma_f32_16x16x32_f16 v[50:53], v[96:99], v[132:135], v[68:71]
	s_nop 2
	ds_read_b128 v[68:71], v59
	v_or_b32_e32 v59, 0x1c800, v57
	v_mfma_f32_16x16x32_f16 v[64:67], v[112:115], v[96:99], v[64:67]
	ds_read_b128 v[96:99], v59
	v_or_b32_e32 v59, 0x1d000, v57
	v_mfma_f32_16x16x32_f16 v[72:75], v[112:115], v[92:95], v[72:75]
	v_or_b32_e32 v112, 0x1d800, v57
	v_mfma_f32_16x16x32_f16 v[92:95], v[92:95], v[132:135], v[120:123]
	v_or_b32_e32 v132, 0x1e800, v57
	s_waitcnt vmcnt(11) lgkmcnt(1)
	v_mfma_f32_16x16x32_f16 v[100:103], v[46:49], v[68:71], v[100:103]
	v_or_b32_e32 v120, 0x1c800, v58
	s_waitcnt vmcnt(10)
	v_mfma_f32_16x16x32_f16 v[104:107], v[42:45], v[68:71], v[104:107]
	s_waitcnt vmcnt(9)
	v_mfma_f32_16x16x32_f16 v[68:71], v[68:71], v[14:17], v[76:79]
	s_waitcnt lgkmcnt(0)
	v_mfma_f32_16x16x32_f16 v[76:79], v[46:49], v[96:99], v[80:83]
	s_nop 2
	ds_read_b128 v[80:83], v59
	ds_read_b128 v[112:115], v112
	v_or_b32_e32 v59, 0x1c000, v58
	ds_read_b128 v[116:119], v59
	ds_read_b128 v[120:123], v120
	v_or_b32_e32 v59, 0x1d000, v58
	v_mfma_f32_16x16x32_f16 v[84:87], v[42:45], v[96:99], v[84:87]
	v_mfma_f32_16x16x32_f16 v[88:91], v[96:99], v[14:17], v[88:91]
	ds_read_b128 v[96:99], v59
	ds_read_b128 v[124:127], v124
	v_or_b32_e32 v59, 0x1e000, v57
	s_waitcnt lgkmcnt(0)
.Lproj_poll_15:
	ds_read_b128 v[160:163], v164
	s_waitcnt lgkmcnt(0)
	v_min_u32_e32 v160, v160, v161
	v_min3_u32 v160, v160, v162, v163
	s_nop 0
	v_readfirstlane_b32 s20, v160
	s_nop 1
	s_cmp_ge_u32 s20, 16
	s_cbranch_scc1 .Lproj_go_15
	s_sleep 2
	s_branch .Lproj_poll_15
.Lproj_go_15:
	s_waitcnt vmcnt(8)
	v_mfma_f32_16x16x32_f16 v[100:103], v[10:13], v[116:119], v[100:103]
	ds_read_b128 v[128:131], v59
	ds_read_b128 v[132:135], v132
	v_or_b32_e32 v59, 0x1f000, v57
	v_or_b32_e32 v57, 0x1f800, v57
	s_waitcnt vmcnt(7)
	v_mfma_f32_16x16x32_f16 v[104:107], v[6:9], v[116:119], v[104:107]
	ds_read_b128 v[136:139], v59
	ds_read_b128 v[140:143], v57
	v_or_b32_e32 v57, 0x1e000, v58
	v_or_b32_e32 v59, 0x1e800, v58
	s_waitcnt vmcnt(6)
	v_mfma_f32_16x16x32_f16 v[68:71], v[116:119], v[2:5], v[68:71]
	ds_read_b128 v[116:119], v57
	ds_read_b128 v[144:147], v59
	v_or_b32_e32 v57, 0x1f000, v58
	v_or_b32_e32 v58, 0x1f800, v58
	s_waitcnt vmcnt(5) lgkmcnt(5)
	v_mfma_f32_16x16x32_f16 v[100:103], v[38:41], v[128:131], v[100:103]
	ds_read_b128 v[148:151], v57
	ds_read_b128 v[152:155], v58
	v_lshl_add_u64 v[58:59], s[4:5], 0, v[54:55]
	v_and_b32_e32 v54, 48, v0
	s_waitcnt vmcnt(4)
	v_mfma_f32_16x16x32_f16 v[104:107], v[34:37], v[128:131], v[104:107]
	s_lshl_b32 s4, s16, 5
	s_waitcnt vmcnt(3)
	v_mfma_f32_16x16x32_f16 v[68:71], v[128:131], v[30:33], v[68:71]
	v_lshl_add_u64 v[128:129], v[58:59], 0, v[54:55]
	s_waitcnt vmcnt(2) lgkmcnt(3)
	v_mfma_f32_16x16x32_f16 v[100:103], v[22:25], v[116:119], v[100:103]
	s_waitcnt vmcnt(1)
	v_mfma_f32_16x16x32_f16 v[104:107], v[26:29], v[116:119], v[104:107]
	s_waitcnt vmcnt(0)
	v_mfma_f32_16x16x32_f16 v[68:71], v[116:119], v[18:21], v[68:71]
	s_nop 3
	v_mov_b32_e32 v54, v101
	v_mov_b32_e32 v55, v102
	v_pk_mul_f32 v[54:55], v[54:55], s[2:3] op_sel_hi:[1,0]
	v_mfma_f32_16x16x32_f16 v[76:79], v[10:13], v[120:123], v[76:79]
	v_fma_mixlo_f16 v57, v100, s2, 0
	v_cvt_pk_f16_f32 v100, v54, v55
	v_mov_b32_e32 v54, v105
	v_mov_b32_e32 v55, v106
	v_mfma_f32_16x16x32_f16 v[84:87], v[6:9], v[120:123], v[84:87]
	v_mul_f32_e64 v54, v54, s2
	v_mul_f32_e64 v55, v55, s2
	v_pack_b32_f16 v58, v57, v100
	v_cvt_pk_f16_f32 v57, v54, v55
	v_mov_b32_e32 v54, v69
	v_mfma_f32_16x16x32_f16 v[88:91], v[120:123], v[2:5], v[88:91]
	v_mov_b32_e32 v55, v70
	v_pk_mul_f32 v[54:55], v[54:55], s[2:3] op_sel_hi:[1,0]
	v_fma_mixlo_f16 v59, v104, s2, 0
	v_mfma_f32_16x16x32_f16 v[76:79], v[38:41], v[132:135], v[76:79]
	v_cvt_pk_f16_f32 v70, v54, v55
	v_fma_mixlo_f16 v54, v103, s2, 0
	v_fma_mixlo_f16 v104, v68, s2, 0
	v_mfma_f32_16x16x32_f16 v[84:87], v[34:37], v[132:135], v[84:87]
	v_pack_b32_f16 v68, v59, v57
	v_alignbit_b32 v59, v54, v100, 16
	v_fma_mixlo_f16 v54, v107, s2, 0
	v_alignbit_b32 v69, v54, v57, 16
	v_lshlrev_b64 v[100:101], 7, v[156:157]
	v_mfma_f32_16x16x32_f16 v[88:91], v[132:135], v[30:33], v[88:91]
	v_lshl_or_b32 v105, v56, 3, s4
	v_or_b32_e32 v100, v100, v105
	v_lshl_add_u64 v[102:103], s[6:7], 0, v[100:101]
	s_waitcnt lgkmcnt(2)
	v_mfma_f32_16x16x32_f16 v[54:57], v[22:25], v[144:147], v[76:79]
	global_store_dwordx2 v[102:103], v[58:59], off
	v_lshl_add_u64 v[58:59], s[8:9], 0, v[100:101]
	global_store_dwordx2 v[58:59], v[68:69], off
	v_mfma_f32_16x16x32_f16 v[76:79], v[26:29], v[144:147], v[84:87]
	v_or_b32_e32 v68, 16, v156
	s_nop 2
	v_fma_mixlo_f16 v58, v54, s2, 0
	v_mov_b32_e32 v54, v55
	v_mfma_f32_16x16x32_f16 v[84:87], v[144:147], v[18:21], v[88:91]
	v_mov_b32_e32 v55, v56
	v_pk_mul_f32 v[54:55], v[54:55], s[2:3] op_sel_hi:[1,0]
	v_fma_mixlo_f16 v59, v76, s2, 0
	v_mfma_f32_16x16x32_f16 v[60:63], v[46:49], v[80:83], v[60:63]
	v_cvt_pk_f16_f32 v56, v54, v55
	v_mov_b32_e32 v54, v77
	v_mov_b32_e32 v55, v78
	v_mfma_f32_16x16x32_f16 v[72:75], v[42:45], v[80:83], v[72:75]
	v_mul_f32_e64 v54, v54, s2
	v_mul_f32_e64 v55, v55, s2
	v_pack_b32_f16 v76, v58, v56
	v_ashrrev_i32_e32 v69, 31, v68
	v_mfma_f32_16x16x32_f16 v[80:83], v[80:83], v[14:17], v[92:95]
	v_lshlrev_b64 v[68:69], 7, v[68:69]
	v_or_b32_e32 v68, v68, v105
	v_fma_mixlo_f16 v84, v84, s2, 0
	v_mfma_f32_16x16x32_f16 v[42:45], v[42:45], v[112:115], v[64:67]
	s_nop 2
	v_cvt_pk_f16_f32 v67, v54, v55
	v_mov_b32_e32 v54, v85
	v_mov_b32_e32 v55, v86
	v_pk_mul_f32 v[54:55], v[54:55], s[2:3] op_sel_hi:[1,0]
	v_pack_b32_f16 v66, v59, v67
	v_mfma_f32_16x16x32_f16 v[58:61], v[10:13], v[96:99], v[60:63]
	v_mfma_f32_16x16x32_f16 v[62:65], v[6:9], v[96:99], v[72:75]
	s_nop 2
	v_cvt_pk_f16_f32 v74, v54, v55
	v_fma_mixlo_f16 v54, v57, s2, 0
	v_alignbit_b32 v77, v54, v56, 16
	v_mfma_f32_16x16x32_f16 v[54:57], v[96:99], v[2:5], v[80:83]
	v_fma_mixlo_f16 v72, v79, s2, 0
	v_alignbit_b32 v67, v72, v67, 16
	v_lshl_add_u64 v[72:73], s[6:7], 0, v[68:69]
	v_mfma_f32_16x16x32_f16 v[46:49], v[46:49], v[112:115], v[108:111]
	v_lshl_add_u64 v[68:69], s[8:9], 0, v[68:69]
	global_store_dwordx2 v[68:69], v[66:67], off
	v_lshrrev_b32_e32 v67, 16, v70
	v_mfma_f32_16x16x32_f16 v[58:61], v[38:41], v[136:139], v[58:61]
	v_lshrrev_b32_e32 v69, 16, v74
	v_fma_mixhi_f16 v69, v87, s2, 0
	v_fma_mixhi_f16 v67, v71, s2, 0
	v_mfma_f32_16x16x32_f16 v[54:57], v[136:139], v[30:33], v[54:57]
	v_pack_b32_f16 v68, v84, v74
	v_pack_b32_f16 v66, v104, v70
	global_store_dwordx4 v[128:129], v[66:69], off
	v_mfma_f32_16x16x32_f16 v[62:65], v[34:37], v[136:139], v[62:65]
	global_store_dwordx2 v[72:73], v[76:77], off
	v_or_b32_e32 v66, 32, v156
	v_ashrrev_i32_e32 v67, 31, v66
	v_mfma_f32_16x16x32_f16 v[14:17], v[112:115], v[14:17], v[50:53]
	v_mfma_f32_16x16x32_f16 v[6:9], v[6:9], v[124:127], v[42:45]
	s_waitcnt lgkmcnt(1)
	v_mfma_f32_16x16x32_f16 v[58:61], v[22:25], v[148:151], v[58:61]
	v_mfma_f32_16x16x32_f16 v[54:57], v[148:151], v[18:21], v[54:57]
	v_mfma_f32_16x16x32_f16 v[10:13], v[10:13], v[124:127], v[46:49]
	s_nop 5
	v_fma_mixlo_f16 v68, v58, s2, 0
	v_mov_b32_e32 v58, v59
	v_mov_b32_e32 v59, v60
	v_mfma_f32_16x16x32_f16 v[62:65], v[26:29], v[148:151], v[62:65]
	v_mul_f32_e64 v50, v58, s2
	v_mul_f32_e64 v51, v59, s2
	v_fma_mixlo_f16 v54, v54, s2, 0
	v_cvt_pk_f16_f32 v50, v50, v51
	v_mfma_f32_16x16x32_f16 v[2:5], v[124:127], v[2:5], v[14:17]
	v_pack_b32_f16 v46, v68, v50
	s_nop 1
	v_mov_b32_e32 v48, v63
	v_mov_b32_e32 v49, v64
	v_mfma_f32_16x16x32_f16 v[6:9], v[34:37], v[140:143], v[6:9]
	v_mov_b32_e32 v14, v55
	v_mov_b32_e32 v15, v56
	v_pk_mul_f32 v[14:15], v[14:15], s[2:3] op_sel_hi:[1,0]
	v_mfma_f32_16x16x32_f16 v[10:13], v[38:41], v[140:143], v[10:13]
	v_mul_f32_e64 v42, v48, s2
	v_mul_f32_e64 v43, v49, s2
	v_cvt_pk_f16_f32 v38, v14, v15
	v_fma_mixlo_f16 v14, v61, s2, 0
	v_mfma_f32_16x16x32_f16 v[2:5], v[140:143], v[30:33], v[2:5]
	v_fma_mixlo_f16 v62, v62, s2, 0
	v_cvt_pk_f16_f32 v43, v42, v43
	v_alignbit_b32 v47, v14, v50, 16
	v_fma_mixlo_f16 v14, v65, s2, 0
	s_waitcnt lgkmcnt(0)
	v_mfma_f32_16x16x32_f16 v[6:9], v[26:29], v[152:155], v[6:9]
	v_pack_b32_f16 v42, v62, v43
	v_alignbit_b32 v43, v14, v43, 16
	v_lshlrev_b64 v[14:15], 7, v[66:67]
	v_mfma_f32_16x16x32_f16 v[10:13], v[22:25], v[152:155], v[10:13]
	v_or_b32_e32 v14, v14, v105
	v_lshl_add_u64 v[16:17], s[6:7], 0, v[14:15]
	global_store_dwordx2 v[16:17], v[46:47], off
	v_mfma_f32_16x16x32_f16 v[2:5], v[152:155], v[18:21], v[2:5]
	v_lshl_add_u64 v[14:15], s[8:9], 0, v[14:15]
	v_fma_mixlo_f16 v17, v6, s2, 0
	v_mov_b32_e32 v6, v7
	v_mov_b32_e32 v7, v8
	global_store_dwordx2 v[14:15], v[42:43], off
	v_or_b32_e32 v14, 48, v156
	v_fma_mixlo_f16 v16, v10, s2, 0
	v_mov_b32_e32 v10, v11
	v_mov_b32_e32 v11, v12
	v_pk_mul_f32 v[6:7], v[6:7], s[2:3] op_sel_hi:[1,0]
	v_ashrrev_i32_e32 v15, 31, v14
	v_pk_mul_f32 v[10:11], v[10:11], s[2:3] op_sel_hi:[1,0]
	v_cvt_pk_f16_f32 v7, v6, v7
	v_fma_mixlo_f16 v8, v9, s2, 0
	v_cvt_pk_f16_f32 v12, v10, v11
	v_pack_b32_f16 v6, v17, v7
	v_mov_b32_e32 v10, v3
	v_mov_b32_e32 v11, v4
	v_alignbit_b32 v7, v8, v7, 16
	v_lshlrev_b64 v[8:9], 7, v[14:15]
	v_pk_mul_f32 v[10:11], v[10:11], s[2:3] op_sel_hi:[1,0]
	v_fma_mixlo_f16 v3, v13, s2, 0
	v_or_b32_e32 v8, v8, v105
	v_fma_mixlo_f16 v18, v2, s2, 0
	v_pack_b32_f16 v2, v16, v12
	v_cvt_pk_f16_f32 v4, v10, v11
	v_alignbit_b32 v3, v3, v12, 16
	v_lshl_add_u64 v[10:11], s[6:7], 0, v[8:9]
	global_store_dwordx2 v[10:11], v[2:3], off
	v_lshl_add_u64 v[2:3], s[8:9], 0, v[8:9]
	global_store_dwordx2 v[2:3], v[6:7], off
	v_lshrrev_b32_e32 v7, 16, v38
	v_lshrrev_b32_e32 v9, 16, v4
	v_fma_mixhi_f16 v9, v5, s2, 0
	v_fma_mixhi_f16 v7, v57, s2, 0
	v_pack_b32_f16 v8, v18, v4
	v_pack_b32_f16 v6, v54, v38
	global_store_dwordx4 v[128:129], v[6:9], off offset:64
	s_cbranch_execnz .LBB1_2
.LBB1_4:
	s_load_dwordx2 s[0:1], s[0:1], 0x0
	v_add_u32_e32 v2, 0xffffff00, v0
	v_ashrrev_i32_e32 v20, 4, v2
	v_add_u32_e32 v2, s12, v20
	v_ashrrev_i32_e32 v3, 31, v2
	v_lshlrev_b64 v[2:3], 12, v[2:3]
	s_lshl_b32 s2, s3, 6
	s_waitcnt lgkmcnt(0)
	v_lshl_add_u64 v[2:3], s[0:1], 0, v[2:3]
	v_lshlrev_b32_e32 v4, 4, v1
	v_mov_b32_e32 v5, 0
	s_and_b32 s6, s2, 0x3c0
	s_mov_b32 s1, 0
	v_lshl_add_u64 v[2:3], v[2:3], 0, v[4:5]
	s_lshl_b32 s0, s6, 2
	v_lshl_add_u64 v[16:17], v[2:3], 0, s[0:1]
	s_mov_b32 s3, 0x10000
	v_add_co_u32_e32 v12, vcc, s3, v16
	s_mov_b32 s4, 0x20000
	s_nop 0
	v_addc_co_u32_e32 v13, vcc, 0, v17, vcc
	global_load_dwordx4 v[4:7], v[16:17], off sc0 sc1 nt
	global_load_dwordx4 v[8:11], v[12:13], off sc0 sc1 nt
	v_add_co_u32_e32 v12, vcc, s4, v16
	s_mov_b32 s5, 0x30000
	s_nop 0
	v_addc_co_u32_e32 v13, vcc, 0, v17, vcc
	s_add_i32 s0, s2, 64
	global_load_dwordx4 v[12:15], v[12:13], off sc0 sc1 nt
	v_add_co_u32_e32 v16, vcc, s5, v16
	s_and_b32 s0, s0, 0x3c0
	s_nop 0
	v_addc_co_u32_e32 v17, vcc, 0, v17, vcc
	s_lshl_b32 s0, s0, 2
	global_load_dwordx4 v[16:19], v[16:17], off sc0 sc1 nt
	v_lshl_add_u64 v[28:29], v[2:3], 0, s[0:1]
	v_lshrrev_b32_e32 v1, 1, v1
	v_lshrrev_b32_e32 v21, 5, v0
	v_lshlrev_b32_e32 v0, 3, v0
	v_add_co_u32_e32 v30, vcc, s3, v28
	v_bitop3_b32 v1, v1, v21, 7 bitop3:0x78
	v_and_b32_e32 v0, 8, v0
	v_addc_co_u32_e32 v31, vcc, 0, v29, vcc
	v_lshl_or_b32 v0, v1, 4, v0
	v_add_co_u32_e32 v36, vcc, s4, v28
	v_lshl_or_b32 v0, v20, 7, v0
	global_load_dwordx4 v[20:23], v[28:29], off sc0 sc1 nt
	global_load_dwordx4 v[24:27], v[30:31], off sc0 sc1 nt
	v_addc_co_u32_e32 v37, vcc, 0, v29, vcc
	s_add_i32 s0, s2, 0x80
	v_add_co_u32_e32 v38, vcc, s5, v28
	s_and_b32 s0, s0, 0x3c0
	s_nop 0
	v_addc_co_u32_e32 v39, vcc, 0, v29, vcc
	global_load_dwordx4 v[28:31], v[36:37], off sc0 sc1 nt
	global_load_dwordx4 v[32:35], v[38:39], off sc0 sc1 nt
	s_lshl_b32 s0, s0, 2
	v_lshl_add_u64 v[44:45], v[2:3], 0, s[0:1]
	v_add_co_u32_e32 v46, vcc, s3, v44
	s_add_i32 s0, s2, 0xc0
	s_nop 0
	v_addc_co_u32_e32 v47, vcc, 0, v45, vcc
	v_add_co_u32_e32 v52, vcc, s4, v44
	global_load_dwordx4 v[36:39], v[44:45], off sc0 sc1 nt
	global_load_dwordx4 v[40:43], v[46:47], off sc0 sc1 nt
	v_addc_co_u32_e32 v53, vcc, 0, v45, vcc
	v_add_co_u32_e32 v54, vcc, s5, v44
	s_and_b32 s0, s0, 0x3c0
	s_nop 0
	v_addc_co_u32_e32 v55, vcc, 0, v45, vcc
	global_load_dwordx4 v[44:47], v[52:53], off sc0 sc1 nt
	global_load_dwordx4 v[48:51], v[54:55], off sc0 sc1 nt
	s_lshl_b32 s0, s0, 2
	v_lshl_add_u64 v[60:61], v[2:3], 0, s[0:1]
	v_add_co_u32_e32 v62, vcc, s3, v60
	s_add_i32 s0, s2, 0x100
	s_nop 0
	v_addc_co_u32_e32 v63, vcc, 0, v61, vcc
	v_add_co_u32_e32 v68, vcc, s4, v60
	global_load_dwordx4 v[52:55], v[60:61], off sc0 sc1 nt
	global_load_dwordx4 v[56:59], v[62:63], off sc0 sc1 nt
	v_addc_co_u32_e32 v69, vcc, 0, v61, vcc
	v_add_co_u32_e32 v70, vcc, s5, v60
	s_and_b32 s0, s0, 0x3c0
	s_nop 0
	v_addc_co_u32_e32 v71, vcc, 0, v61, vcc
	global_load_dwordx4 v[60:63], v[68:69], off sc0 sc1 nt
	global_load_dwordx4 v[64:67], v[70:71], off sc0 sc1 nt
	s_lshl_b32 s0, s0, 2
	v_add_u32_e32 v1, 0x10000, v0
	s_waitcnt vmcnt(15)
	v_cvt_pk_f16_f32 v7, v6, v7
	v_cvt_pk_f16_f32 v6, v4, v5
	s_waitcnt vmcnt(14)
	v_cvt_pk_f16_f32 v5, v10, v11
	v_cvt_pk_f16_f32 v4, v8, v9
	ds_write2st64_b64 v0, v[6:7], v[4:5] offset1:4
	s_waitcnt vmcnt(13)
	v_cvt_pk_f16_f32 v4, v12, v13
	v_lshl_add_u64 v[12:13], v[2:3], 0, s[0:1]
	v_cvt_pk_f16_f32 v5, v14, v15
	v_add_co_u32_e32 v14, vcc, s3, v12
	s_add_i32 s0, s2, 0x140
	s_nop 0
	v_addc_co_u32_e32 v15, vcc, 0, v13, vcc
	s_waitcnt vmcnt(12)
	v_cvt_pk_f16_f32 v7, v18, v19
	v_cvt_pk_f16_f32 v6, v16, v17
	ds_write2st64_b64 v0, v[4:5], v[6:7] offset0:8 offset1:12
	v_add_co_u32_e32 v68, vcc, s4, v12
	global_load_dwordx4 v[4:7], v[12:13], off sc0 sc1 nt
	global_load_dwordx4 v[8:11], v[14:15], off sc0 sc1 nt
	v_addc_co_u32_e32 v69, vcc, 0, v13, vcc
	v_add_co_u32_e32 v70, vcc, s5, v12
	s_and_b32 s0, s0, 0x3c0
	s_nop 0
	v_addc_co_u32_e32 v71, vcc, 0, v13, vcc
	global_load_dwordx4 v[12:15], v[68:69], off sc0 sc1 nt
	global_load_dwordx4 v[16:19], v[70:71], off sc0 sc1 nt
	s_waitcnt vmcnt(15)
	v_cvt_pk_f16_f32 v23, v22, v23
	v_cvt_pk_f16_f32 v22, v20, v21
	s_waitcnt vmcnt(14)
	v_cvt_pk_f16_f32 v21, v26, v27
	v_cvt_pk_f16_f32 v20, v24, v25
	s_lshl_b32 s0, s0, 2
	s_waitcnt lgkmcnt(0)
	v_add_u32_e32 v171, 1, v171
	ds_write_b32 v169, v171
	ds_write2st64_b64 v0, v[22:23], v[20:21] offset0:16 offset1:20
	s_waitcnt vmcnt(13)
	v_cvt_pk_f16_f32 v20, v28, v29
	v_lshl_add_u64 v[28:29], v[2:3], 0, s[0:1]
	v_cvt_pk_f16_f32 v21, v30, v31
	v_add_co_u32_e32 v30, vcc, s3, v28
	s_waitcnt vmcnt(12)
	v_cvt_pk_f16_f32 v23, v34, v35
	v_cvt_pk_f16_f32 v22, v32, v33
	v_addc_co_u32_e32 v31, vcc, 0, v29, vcc
	ds_write2st64_b64 v0, v[20:21], v[22:23] offset0:24 offset1:28
	v_add_co_u32_e32 v68, vcc, s4, v28
	global_load_dwordx4 v[20:23], v[28:29], off sc0 sc1 nt
	global_load_dwordx4 v[24:27], v[30:31], off sc0 sc1 nt
	v_addc_co_u32_e32 v69, vcc, 0, v29, vcc
	s_add_i32 s0, s2, 0x180
	v_add_co_u32_e32 v70, vcc, s5, v28
	s_and_b32 s0, s0, 0x3c0
	s_nop 0
	v_addc_co_u32_e32 v71, vcc, 0, v29, vcc
	global_load_dwordx4 v[28:31], v[68:69], off sc0 sc1 nt
	global_load_dwordx4 v[32:35], v[70:71], off sc0 sc1 nt
	s_waitcnt vmcnt(15)
	v_cvt_pk_f16_f32 v39, v38, v39
	v_cvt_pk_f16_f32 v38, v36, v37
	s_waitcnt vmcnt(14)
	v_cvt_pk_f16_f32 v37, v42, v43
	v_cvt_pk_f16_f32 v36, v40, v41
	s_lshl_b32 s0, s0, 2
	s_waitcnt lgkmcnt(0)
	v_add_u32_e32 v171, 1, v171
	ds_write_b32 v169, v171
	ds_write2st64_b64 v0, v[38:39], v[36:37] offset0:32 offset1:36
	s_waitcnt vmcnt(13)
	v_cvt_pk_f16_f32 v36, v44, v45
	v_lshl_add_u64 v[44:45], v[2:3], 0, s[0:1]
	v_cvt_pk_f16_f32 v37, v46, v47
	v_add_co_u32_e32 v46, vcc, s3, v44
	s_waitcnt vmcnt(12)
	v_cvt_pk_f16_f32 v39, v50, v51
	v_cvt_pk_f16_f32 v38, v48, v49
	v_addc_co_u32_e32 v47, vcc, 0, v45, vcc
	ds_write2st64_b64 v0, v[36:37], v[38:39] offset0:40 offset1:44
	v_add_co_u32_e32 v68, vcc, s4, v44
	global_load_dwordx4 v[36:39], v[44:45], off sc0 sc1 nt
	global_load_dwordx4 v[40:43], v[46:47], off sc0 sc1 nt
	v_addc_co_u32_e32 v69, vcc, 0, v45, vcc
	v_add_co_u32_e32 v70, vcc, s5, v44
	s_add_i32 s0, s2, 0x1c0
	s_nop 0
	v_addc_co_u32_e32 v71, vcc, 0, v45, vcc
	global_load_dwordx4 v[44:47], v[68:69], off sc0 sc1 nt
	global_load_dwordx4 v[48:51], v[70:71], off sc0 sc1 nt
	s_and_b32 s0, s0, 0x3c0
	s_waitcnt vmcnt(15)
	v_cvt_pk_f16_f32 v55, v54, v55
	v_cvt_pk_f16_f32 v54, v52, v53
	s_waitcnt vmcnt(14)
	v_cvt_pk_f16_f32 v53, v58, v59
	v_cvt_pk_f16_f32 v52, v56, v57
	s_lshl_b32 s0, s0, 2
	s_waitcnt lgkmcnt(0)
	v_add_u32_e32 v171, 1, v171
	ds_write_b32 v169, v171
	ds_write2st64_b64 v0, v[54:55], v[52:53] offset0:48 offset1:52
	s_waitcnt vmcnt(13)
	v_cvt_pk_f16_f32 v52, v60, v61
	v_lshl_add_u64 v[60:61], v[2:3], 0, s[0:1]
	v_cvt_pk_f16_f32 v53, v62, v63
	v_add_co_u32_e32 v62, vcc, s3, v60
	s_waitcnt vmcnt(12)
	v_cvt_pk_f16_f32 v55, v66, v67
	v_addc_co_u32_e32 v63, vcc, 0, v61, vcc
	v_cvt_pk_f16_f32 v54, v64, v65
	v_add_co_u32_e32 v68, vcc, s4, v60
	ds_write2st64_b64 v0, v[52:53], v[54:55] offset0:56 offset1:60
	s_nop 0
	v_addc_co_u32_e32 v69, vcc, 0, v61, vcc
	global_load_dwordx4 v[52:55], v[60:61], off sc0 sc1 nt
	global_load_dwordx4 v[56:59], v[62:63], off sc0 sc1 nt
	v_add_co_u32_e32 v70, vcc, s5, v60
	s_xor_b32 s0, s6, 0x200
	s_nop 0
	v_addc_co_u32_e32 v71, vcc, 0, v61, vcc
	global_load_dwordx4 v[60:63], v[68:69], off sc0 sc1 nt
	global_load_dwordx4 v[64:67], v[70:71], off sc0 sc1 nt
	s_waitcnt vmcnt(15)
	v_cvt_pk_f16_f32 v7, v6, v7
	v_cvt_pk_f16_f32 v6, v4, v5
	s_waitcnt vmcnt(14)
	v_cvt_pk_f16_f32 v5, v10, v11
	v_cvt_pk_f16_f32 v4, v8, v9
	s_lshl_b32 s0, s0, 2
	s_waitcnt lgkmcnt(0)
	v_add_u32_e32 v171, 1, v171
	ds_write_b32 v169, v171
	ds_write2st64_b64 v0, v[6:7], v[4:5] offset0:64 offset1:68
	s_waitcnt vmcnt(13)
	v_cvt_pk_f16_f32 v4, v12, v13
	v_lshl_add_u64 v[12:13], v[2:3], 0, s[0:1]
	v_cvt_pk_f16_f32 v5, v14, v15
	v_add_co_u32_e32 v14, vcc, s3, v12
	s_waitcnt vmcnt(12)
	v_cvt_pk_f16_f32 v7, v18, v19
	v_cvt_pk_f16_f32 v6, v16, v17
	v_addc_co_u32_e32 v15, vcc, 0, v13, vcc
	ds_write2st64_b64 v0, v[4:5], v[6:7] offset0:72 offset1:76
	v_add_co_u32_e32 v68, vcc, s4, v12
	global_load_dwordx4 v[4:7], v[12:13], off sc0 sc1 nt
	global_load_dwordx4 v[8:11], v[14:15], off sc0 sc1 nt
	v_addc_co_u32_e32 v69, vcc, 0, v13, vcc
	s_add_i32 s0, s2, 0x240
	v_add_co_u32_e32 v70, vcc, s5, v12
	s_and_b32 s0, s0, 0x3c0
	s_nop 0
	v_addc_co_u32_e32 v71, vcc, 0, v13, vcc
	global_load_dwordx4 v[12:15], v[68:69], off sc0 sc1 nt
	global_load_dwordx4 v[16:19], v[70:71], off sc0 sc1 nt
	s_waitcnt vmcnt(15)
	v_cvt_pk_f16_f32 v23, v22, v23
	v_cvt_pk_f16_f32 v22, v20, v21
	s_waitcnt vmcnt(14)
	v_cvt_pk_f16_f32 v21, v26, v27
	v_cvt_pk_f16_f32 v20, v24, v25
	s_lshl_b32 s0, s0, 2
	s_waitcnt lgkmcnt(0)
	v_add_u32_e32 v171, 1, v171
	ds_write_b32 v169, v171
	ds_write2st64_b64 v0, v[22:23], v[20:21] offset0:80 offset1:84
	s_waitcnt vmcnt(13)
	v_cvt_pk_f16_f32 v20, v28, v29
	v_lshl_add_u64 v[28:29], v[2:3], 0, s[0:1]
	v_cvt_pk_f16_f32 v21, v30, v31
	v_add_co_u32_e32 v30, vcc, s3, v28
	s_waitcnt vmcnt(12)
	v_cvt_pk_f16_f32 v23, v34, v35
	v_cvt_pk_f16_f32 v22, v32, v33
	v_addc_co_u32_e32 v31, vcc, 0, v29, vcc
	ds_write2st64_b64 v0, v[20:21], v[22:23] offset0:88 offset1:92
	v_add_co_u32_e32 v68, vcc, s4, v28
	global_load_dwordx4 v[20:23], v[28:29], off sc0 sc1 nt
	global_load_dwordx4 v[24:27], v[30:31], off sc0 sc1 nt
	v_addc_co_u32_e32 v69, vcc, 0, v29, vcc
	s_add_i32 s0, s2, 0x280
	v_add_co_u32_e32 v70, vcc, s5, v28
	s_and_b32 s0, s0, 0x3c0
	s_nop 0
	v_addc_co_u32_e32 v71, vcc, 0, v29, vcc
	global_load_dwordx4 v[28:31], v[68:69], off sc0 sc1 nt
	global_load_dwordx4 v[32:35], v[70:71], off sc0 sc1 nt
	s_waitcnt vmcnt(15)
	v_cvt_pk_f16_f32 v39, v38, v39
	v_cvt_pk_f16_f32 v38, v36, v37
	s_waitcnt vmcnt(14)
	v_cvt_pk_f16_f32 v37, v42, v43
	v_cvt_pk_f16_f32 v36, v40, v41
	s_lshl_b32 s0, s0, 2
	s_waitcnt lgkmcnt(0)
	v_add_u32_e32 v171, 1, v171
	ds_write_b32 v169, v171
	ds_write2st64_b64 v0, v[38:39], v[36:37] offset0:96 offset1:100
	s_waitcnt vmcnt(13)
	v_cvt_pk_f16_f32 v36, v44, v45
	v_lshl_add_u64 v[44:45], v[2:3], 0, s[0:1]
	v_cvt_pk_f16_f32 v37, v46, v47
	v_add_co_u32_e32 v46, vcc, s3, v44
	s_waitcnt vmcnt(12)
	v_cvt_pk_f16_f32 v39, v50, v51
	v_cvt_pk_f16_f32 v38, v48, v49
	v_addc_co_u32_e32 v47, vcc, 0, v45, vcc
	ds_write2st64_b64 v0, v[36:37], v[38:39] offset0:104 offset1:108
	v_add_co_u32_e32 v68, vcc, s4, v44
	global_load_dwordx4 v[36:39], v[44:45], off sc0 sc1 nt
	global_load_dwordx4 v[40:43], v[46:47], off sc0 sc1 nt
	v_addc_co_u32_e32 v69, vcc, 0, v45, vcc
	v_add_co_u32_e32 v70, vcc, s5, v44
	s_add_i32 s0, s2, 0x2c0
	s_nop 0
	v_addc_co_u32_e32 v71, vcc, 0, v45, vcc
	global_load_dwordx4 v[44:47], v[68:69], off sc0 sc1 nt
	global_load_dwordx4 v[48:51], v[70:71], off sc0 sc1 nt
	s_and_b32 s0, s0, 0x3c0
	s_waitcnt vmcnt(15)
	v_cvt_pk_f16_f32 v55, v54, v55
	v_cvt_pk_f16_f32 v54, v52, v53
	s_waitcnt vmcnt(14)
	v_cvt_pk_f16_f32 v53, v58, v59
	v_cvt_pk_f16_f32 v52, v56, v57
	s_lshl_b32 s0, s0, 2
	s_waitcnt lgkmcnt(0)
	v_add_u32_e32 v171, 1, v171
	ds_write_b32 v169, v171
	ds_write2st64_b64 v0, v[54:55], v[52:53] offset0:112 offset1:116
	s_waitcnt vmcnt(13)
	v_cvt_pk_f16_f32 v53, v62, v63
	v_cvt_pk_f16_f32 v52, v60, v61
	s_waitcnt vmcnt(12)
	v_cvt_pk_f16_f32 v55, v66, v67
	v_cvt_pk_f16_f32 v54, v64, v65
	v_lshl_add_u64 v[60:61], v[2:3], 0, s[0:1]
	ds_write2st64_b64 v0, v[52:53], v[54:55] offset0:120 offset1:124
	v_add_co_u32_e32 v62, vcc, s3, v60
	s_add_i32 s0, s2, 0x300
	s_nop 0
	v_addc_co_u32_e32 v63, vcc, 0, v61, vcc
	global_load_dwordx4 v[52:55], v[60:61], off sc0 sc1 nt
	global_load_dwordx4 v[56:59], v[62:63], off sc0 sc1 nt
	v_add_co_u32_e32 v68, vcc, s4, v60
	s_waitcnt vmcnt(13)
	v_cvt_pk_f16_f32 v7, v6, v7
	v_addc_co_u32_e32 v69, vcc, 0, v61, vcc
	v_add_co_u32_e32 v70, vcc, s5, v60
	v_cvt_pk_f16_f32 v6, v4, v5
	s_and_b32 s0, s0, 0x3c0
	v_addc_co_u32_e32 v71, vcc, 0, v61, vcc
	global_load_dwordx4 v[60:63], v[68:69], off sc0 sc1 nt
	global_load_dwordx4 v[64:67], v[70:71], off sc0 sc1 nt
	s_waitcnt lgkmcnt(0)
	v_add_u32_e32 v171, 1, v171
	ds_write_b32 v169, v171
	ds_write_b64 v1, v[6:7]
	s_waitcnt vmcnt(14)
	v_cvt_pk_f16_f32 v5, v10, v11
	v_cvt_pk_f16_f32 v4, v8, v9
	v_add_u32_e32 v1, 0x10800, v0
	s_lshl_b32 s0, s0, 2
	ds_write_b64 v1, v[4:5]
	s_waitcnt vmcnt(13)
	v_cvt_pk_f16_f32 v4, v12, v13
	v_lshl_add_u64 v[12:13], v[2:3], 0, s[0:1]
	v_cvt_pk_f16_f32 v5, v14, v15
	v_add_co_u32_e32 v14, vcc, s3, v12
	v_add_u32_e32 v1, 0x11000, v0
	s_nop 0
	v_addc_co_u32_e32 v15, vcc, 0, v13, vcc
	v_add_co_u32_e32 v68, vcc, s4, v12
	ds_write_b64 v1, v[4:5]
	s_waitcnt vmcnt(12)
	v_cvt_pk_f16_f32 v5, v18, v19
	v_cvt_pk_f16_f32 v4, v16, v17
	v_add_u32_e32 v1, 0x11800, v0
	v_addc_co_u32_e32 v69, vcc, 0, v13, vcc
	s_add_i32 s0, s2, 0x340
	ds_write_b64 v1, v[4:5]
	v_add_co_u32_e32 v70, vcc, s5, v12
	s_waitcnt vmcnt(11)
	v_cvt_pk_f16_f32 v23, v22, v23
	v_cvt_pk_f16_f32 v22, v20, v21
	v_add_u32_e32 v1, 0x12000, v0
	s_and_b32 s0, s0, 0x3c0
	global_load_dwordx4 v[4:7], v[12:13], off sc0 sc1 nt
	global_load_dwordx4 v[8:11], v[14:15], off sc0 sc1 nt
	v_addc_co_u32_e32 v71, vcc, 0, v13, vcc
	global_load_dwordx4 v[12:15], v[68:69], off sc0 sc1 nt
	global_load_dwordx4 v[16:19], v[70:71], off sc0 sc1 nt
	s_waitcnt lgkmcnt(0)
	v_add_u32_e32 v171, 1, v171
	ds_write_b32 v169, v171
	ds_write_b64 v1, v[22:23]
	s_waitcnt vmcnt(14)
	v_cvt_pk_f16_f32 v21, v26, v27
	v_cvt_pk_f16_f32 v20, v24, v25
	v_add_u32_e32 v1, 0x12800, v0
	s_lshl_b32 s0, s0, 2
	ds_write_b64 v1, v[20:21]
	s_waitcnt vmcnt(13)
	v_cvt_pk_f16_f32 v20, v28, v29
	v_lshl_add_u64 v[28:29], v[2:3], 0, s[0:1]
	v_cvt_pk_f16_f32 v21, v30, v31
	v_add_co_u32_e32 v30, vcc, s3, v28
	v_add_u32_e32 v1, 0x13000, v0
	s_nop 0
	v_addc_co_u32_e32 v31, vcc, 0, v29, vcc
	v_add_co_u32_e32 v68, vcc, s4, v28
	ds_write_b64 v1, v[20:21]
	s_waitcnt vmcnt(12)
	v_cvt_pk_f16_f32 v21, v34, v35
	v_cvt_pk_f16_f32 v20, v32, v33
	v_add_u32_e32 v1, 0x13800, v0
	v_addc_co_u32_e32 v69, vcc, 0, v29, vcc
	s_add_i32 s0, s2, 0x380
	ds_write_b64 v1, v[20:21]
	v_add_co_u32_e32 v70, vcc, s5, v28
	s_waitcnt vmcnt(11)
	v_cvt_pk_f16_f32 v39, v38, v39
	v_cvt_pk_f16_f32 v38, v36, v37
	v_add_u32_e32 v1, 0x14000, v0
	s_and_b32 s0, s0, 0x3c0
	global_load_dwordx4 v[20:23], v[28:29], off sc0 sc1 nt
	global_load_dwordx4 v[24:27], v[30:31], off sc0 sc1 nt
	v_addc_co_u32_e32 v71, vcc, 0, v29, vcc
	global_load_dwordx4 v[28:31], v[68:69], off sc0 sc1 nt
	global_load_dwordx4 v[32:35], v[70:71], off sc0 sc1 nt
	s_waitcnt lgkmcnt(0)
	v_add_u32_e32 v171, 1, v171
	ds_write_b32 v169, v171
	ds_write_b64 v1, v[38:39]
	s_waitcnt vmcnt(14)
	v_cvt_pk_f16_f32 v37, v42, v43
	v_cvt_pk_f16_f32 v36, v40, v41
	v_add_u32_e32 v1, 0x14800, v0
	s_lshl_b32 s0, s0, 2
	ds_write_b64 v1, v[36:37]
	s_waitcnt vmcnt(13)
	v_cvt_pk_f16_f32 v36, v44, v45
	v_lshl_add_u64 v[44:45], v[2:3], 0, s[0:1]
	v_cvt_pk_f16_f32 v37, v46, v47
	v_add_co_u32_e32 v46, vcc, s3, v44
	s_addk_i32 s2, 0x3c0
	s_nop 0
	v_addc_co_u32_e32 v47, vcc, 0, v45, vcc
	v_add_co_u32_e32 v68, vcc, s4, v44
	v_add_u32_e32 v1, 0x15000, v0
	s_nop 0
	v_addc_co_u32_e32 v69, vcc, 0, v45, vcc
	s_and_b32 s0, s2, 0x3c0
	ds_write_b64 v1, v[36:37]
	s_waitcnt vmcnt(12)
	v_cvt_pk_f16_f32 v37, v50, v51
	v_cvt_pk_f16_f32 v36, v48, v49
	v_add_u32_e32 v1, 0x15800, v0
	v_add_co_u32_e32 v70, vcc, s5, v44
	s_lshl_b32 s0, s0, 2
	ds_write_b64 v1, v[36:37]
	v_addc_co_u32_e32 v71, vcc, 0, v45, vcc
	v_lshl_add_u64 v[2:3], v[2:3], 0, s[0:1]
	global_load_dwordx4 v[36:39], v[44:45], off sc0 sc1 nt
	global_load_dwordx4 v[40:43], v[46:47], off sc0 sc1 nt
	s_waitcnt vmcnt(13)
	v_cvt_pk_f16_f32 v55, v54, v55
	v_cvt_pk_f16_f32 v54, v52, v53
	s_waitcnt vmcnt(12)
	v_cvt_pk_f16_f32 v52, v56, v57
	v_add_co_u32_e32 v56, vcc, s3, v2
	v_add_u32_e32 v1, 0x16000, v0
	s_nop 0
	v_addc_co_u32_e32 v57, vcc, 0, v3, vcc
	global_load_dwordx4 v[44:47], v[68:69], off sc0 sc1 nt
	global_load_dwordx4 v[48:51], v[70:71], off sc0 sc1 nt
	s_waitcnt lgkmcnt(0)
	v_add_u32_e32 v171, 1, v171
	ds_write_b32 v169, v171
	ds_write_b64 v1, v[54:55]
	v_cvt_pk_f16_f32 v53, v58, v59
	v_add_u32_e32 v1, 0x16800, v0
	v_add_co_u32_e32 v68, vcc, s4, v2
	ds_write_b64 v1, v[52:53]
	global_load_dwordx4 v[52:55], v[2:3], off sc0 sc1 nt
	v_addc_co_u32_e32 v69, vcc, 0, v3, vcc
	global_load_dwordx4 v[56:59], v[56:57], off sc0 sc1 nt
	v_add_co_u32_e32 v2, vcc, s5, v2
	global_load_dwordx4 v[68:71], v[68:69], off sc0 sc1 nt
	s_nop 0
	v_addc_co_u32_e32 v3, vcc, 0, v3, vcc
	global_load_dwordx4 v[72:75], v[2:3], off sc0 sc1 nt
	s_waitcnt vmcnt(17)
	v_cvt_pk_f16_f32 v63, v62, v63
	v_cvt_pk_f16_f32 v62, v60, v61
	v_add_u32_e32 v1, 0x17000, v0
	ds_write_b64 v1, v[62:63]
	s_waitcnt vmcnt(16)
	v_cvt_pk_f16_f32 v3, v66, v67
	v_cvt_pk_f16_f32 v2, v64, v65
	v_add_u32_e32 v1, 0x17800, v0
	ds_write_b64 v1, v[2:3]
	s_waitcnt vmcnt(15)
	v_cvt_pk_f16_f32 v3, v6, v7
	v_cvt_pk_f16_f32 v2, v4, v5
	v_add_u32_e32 v1, 0x18000, v0
	s_waitcnt lgkmcnt(0)
	v_add_u32_e32 v171, 1, v171
	ds_write_b32 v169, v171
	ds_write_b64 v1, v[2:3]
	s_waitcnt vmcnt(14)
	v_cvt_pk_f16_f32 v3, v10, v11
	v_cvt_pk_f16_f32 v2, v8, v9
	v_add_u32_e32 v1, 0x18800, v0
	ds_write_b64 v1, v[2:3]
	s_waitcnt vmcnt(13)
	v_cvt_pk_f16_f32 v3, v14, v15
	v_cvt_pk_f16_f32 v2, v12, v13
	v_add_u32_e32 v1, 0x19000, v0
	ds_write_b64 v1, v[2:3]
	s_waitcnt vmcnt(12)
	v_cvt_pk_f16_f32 v3, v18, v19
	v_cvt_pk_f16_f32 v2, v16, v17
	v_add_u32_e32 v1, 0x19800, v0
	ds_write_b64 v1, v[2:3]
	s_waitcnt vmcnt(11)
	v_cvt_pk_f16_f32 v3, v22, v23
	v_cvt_pk_f16_f32 v2, v20, v21
	v_add_u32_e32 v1, 0x1a000, v0
	s_waitcnt lgkmcnt(0)
	v_add_u32_e32 v171, 1, v171
	ds_write_b32 v169, v171
	ds_write_b64 v1, v[2:3]
	s_waitcnt vmcnt(10)
	v_cvt_pk_f16_f32 v3, v26, v27
	v_cvt_pk_f16_f32 v2, v24, v25
	v_add_u32_e32 v1, 0x1a800, v0
	ds_write_b64 v1, v[2:3]
	s_waitcnt vmcnt(9)
	v_cvt_pk_f16_f32 v3, v30, v31
	v_cvt_pk_f16_f32 v2, v28, v29
	v_add_u32_e32 v1, 0x1b000, v0
	ds_write_b64 v1, v[2:3]
	s_waitcnt vmcnt(8)
	v_cvt_pk_f16_f32 v3, v34, v35
	v_cvt_pk_f16_f32 v2, v32, v33
	v_add_u32_e32 v1, 0x1b800, v0
	ds_write_b64 v1, v[2:3]
	v_add_u32_e32 v1, 0x1c000, v0
	s_waitcnt lgkmcnt(0)
	v_add_u32_e32 v171, 1, v171
	ds_write_b32 v169, v171
	s_waitcnt vmcnt(7)
	v_cvt_pk_f16_f32 v3, v38, v39
	v_cvt_pk_f16_f32 v2, v36, v37
	ds_write_b64 v1, v[2:3]
	s_waitcnt vmcnt(6)
	v_cvt_pk_f16_f32 v3, v42, v43
	v_cvt_pk_f16_f32 v2, v40, v41
	v_add_u32_e32 v1, 0x1c800, v0
	ds_write_b64 v1, v[2:3]
	v_add_u32_e32 v1, 0x1d000, v0
	s_waitcnt vmcnt(5)
	v_cvt_pk_f16_f32 v3, v46, v47
	v_cvt_pk_f16_f32 v2, v44, v45
	ds_write_b64 v1, v[2:3]
	s_waitcnt vmcnt(4)
	v_cvt_pk_f16_f32 v3, v50, v51
	v_cvt_pk_f16_f32 v2, v48, v49
	v_add_u32_e32 v1, 0x1d800, v0
	ds_write_b64 v1, v[2:3]
	v_add_u32_e32 v1, 0x1e000, v0
	s_waitcnt lgkmcnt(0)
	v_add_u32_e32 v171, 1, v171
	ds_write_b32 v169, v171
	s_waitcnt vmcnt(3)
	v_cvt_pk_f16_f32 v3, v54, v55
	v_cvt_pk_f16_f32 v2, v52, v53
	ds_write_b64 v1, v[2:3]
	s_waitcnt vmcnt(2)
	v_cvt_pk_f16_f32 v3, v58, v59
	v_cvt_pk_f16_f32 v2, v56, v57
	v_add_u32_e32 v1, 0x1e800, v0
	ds_write_b64 v1, v[2:3]
	s_waitcnt vmcnt(1)
	v_cvt_pk_f16_f32 v3, v70, v71
	v_cvt_pk_f16_f32 v2, v68, v69
	v_add_u32_e32 v1, 0x1f000, v0
	ds_write_b64 v1, v[2:3]
	s_waitcnt vmcnt(0)
	v_cvt_pk_f16_f32 v3, v74, v75
	v_cvt_pk_f16_f32 v2, v72, v73
	v_add_u32_e32 v0, 0x1f800, v0
	ds_write_b64 v0, v[2:3]
	s_waitcnt lgkmcnt(0)
	v_add_u32_e32 v171, 1, v171
	ds_write_b32 v169, v171
	s_waitcnt lgkmcnt(0)
	s_endpgm

	.amdhsa_kernel _Z11proj_kernelPKfPKDv8_DF16_PDF16_S4_S4_
		.amdhsa_group_segment_fixed_size 131328
		.amdhsa_private_segment_fixed_size 0
		.amdhsa_kernarg_size 40
		.amdhsa_user_sgpr_count 2
		.amdhsa_user_sgpr_dispatch_ptr 0
		.amdhsa_user_sgpr_queue_ptr 0
		.amdhsa_user_sgpr_kernarg_segment_ptr 1
		.amdhsa_user_sgpr_dispatch_id 0
		.amdhsa_user_sgpr_kernarg_preload_length 0
		.amdhsa_user_sgpr_kernarg_preload_offset 0
		.amdhsa_user_sgpr_private_segment_size 0
		.amdhsa_uses_dynamic_stack 0
		.amdhsa_enable_private_segment 0
		.amdhsa_system_sgpr_workgroup_id_x 1
		.amdhsa_system_sgpr_workgroup_id_y 0
		.amdhsa_system_sgpr_workgroup_id_z 0
		.amdhsa_system_sgpr_workgroup_info 0
		.amdhsa_system_vgpr_workitem_id 0
		.amdhsa_next_free_vgpr 176
		.amdhsa_next_free_sgpr 96
		.amdhsa_accum_offset 176
		.amdhsa_reserve_vcc 1
		.amdhsa_float_round_mode_32 0
		.amdhsa_float_round_mode_16_64 0
		.amdhsa_float_denorm_mode_32 3
		.amdhsa_float_denorm_mode_16_64 3
		.amdhsa_dx10_clamp 1
		.amdhsa_ieee_mode 1
		.amdhsa_fp16_overflow 0
		.amdhsa_tg_split 0
		.amdhsa_exception_fp_ieee_invalid_op 0
		.amdhsa_exception_fp_denorm_src 0
		.amdhsa_exception_fp_ieee_div_zero 0
		.amdhsa_exception_fp_ieee_overflow 0
		.amdhsa_exception_fp_ieee_underflow 0
		.amdhsa_exception_fp_ieee_inexact 0
		.amdhsa_exception_int_div_zero 0
	.end_amdhsa_kernel

amdhsa.kernels:
  - .agpr_count:     0
    .args:
      - .actual_access:  read_only
        .address_space:  global
        .offset:         0
        .size:           8
        .value_kind:     global_buffer
      - .actual_access:  read_only
        .address_space:  global
        .offset:         8
        .size:           8
        .value_kind:     global_buffer
      - .actual_access:  read_only
        .address_space:  global
        .offset:         16
        .size:           8
        .value_kind:     global_buffer
      - .actual_access:  write_only
        .address_space:  global
        .offset:         24
        .size:           8
        .value_kind:     global_buffer
      - .offset:         32
        .size:           4
        .value_kind:     hidden_block_count_x
      - .offset:         36
        .size:           4
        .value_kind:     hidden_block_count_y
      - .offset:         40
        .size:           4
        .value_kind:     hidden_block_count_z
      - .offset:         44
        .size:           2
        .value_kind:     hidden_group_size_x
      - .offset:         46
        .size:           2
        .value_kind:     hidden_group_size_y
      - .offset:         48
        .size:           2
        .value_kind:     hidden_group_size_z
      - .offset:         50
        .size:           2
        .value_kind:     hidden_remainder_x
      - .offset:         52
        .size:           2
        .value_kind:     hidden_remainder_y
      - .offset:         54
        .size:           2
        .value_kind:     hidden_remainder_z
      - .offset:         72
        .size:           8
        .value_kind:     hidden_global_offset_x
      - .offset:         80
        .size:           8
        .value_kind:     hidden_global_offset_y
      - .offset:         88
        .size:           8
        .value_kind:     hidden_global_offset_z
      - .offset:         96
        .size:           2
        .value_kind:     hidden_grid_dims
    .group_segment_fixed_size: 0
    .kernarg_segment_align: 8
    .kernarg_segment_size: 288
    .language:       OpenCL C
    .language_version:
      - 2
      - 0
    .max_flat_workgroup_size: 1024
    .name:           _Z13prep_w_kernelPKfS0_S0_PDv8_DF16_
    .private_segment_fixed_size: 0
    .sgpr_count:     18
    .sgpr_spill_count: 0
    .symbol:         _Z13prep_w_kernelPKfS0_S0_PDv8_DF16_.kd
    .uniform_work_group_size: 1
    .uses_dynamic_stack: false
    .vgpr_count:     15
    .vgpr_spill_count: 0
    .wavefront_size: 64
  - .agpr_count:     0
    .args:
      - .actual_access:  read_only
        .address_space:  global
        .offset:         0
        .size:           8
        .value_kind:     global_buffer
      - .actual_access:  read_only
        .address_space:  global
        .offset:         8
        .size:           8
        .value_kind:     global_buffer
      - .actual_access:  write_only
        .address_space:  global
        .offset:         16
        .size:           8
        .value_kind:     global_buffer
      - .actual_access:  write_only
        .address_space:  global
        .offset:         24
        .size:           8
        .value_kind:     global_buffer
      - .actual_access:  write_only
        .address_space:  global
        .offset:         32
        .size:           8
        .value_kind:     global_buffer
    .group_segment_fixed_size: 131328
    .kernarg_segment_align: 8
    .kernarg_segment_size: 40
    .language:       OpenCL C
    .language_version:
      - 2
      - 0
    .max_flat_workgroup_size: 512
    .name:           _Z11proj_kernelPKfPKDv8_DF16_PDF16_S4_S4_
    .private_segment_fixed_size: 0
    .sgpr_count:     26
    .sgpr_spill_count: 0
    .symbol:         _Z11proj_kernelPKfPKDv8_DF16_PDF16_S4_S4_.kd
    .uniform_work_group_size: 1
    .uses_dynamic_stack: false
    .vgpr_count:     176
    .vgpr_spill_count: 0
    .wavefront_size: 64
  - .agpr_count:     0
    .args:
      - .actual_access:  read_only
        .address_space:  global
        .offset:         0
        .size:           8
        .value_kind:     global_buffer
      - .address_space:  global
        .offset:         8
        .size:           8
        .value_kind:     global_buffer
      - .address_space:  global
        .offset:         16
        .size:           8
        .value_kind:     global_buffer
      - .actual_access:  write_only
        .address_space:  global
        .offset:         24
        .size:           8
        .value_kind:     global_buffer
      - .actual_access:  write_only
        .address_space:  global
        .offset:         32
        .size:           8
        .value_kind:     global_buffer
      - .actual_access:  write_only
        .address_space:  global
        .offset:         40
        .size:           8
        .value_kind:     global_buffer
    .group_segment_fixed_size: 65536
    .kernarg_segment_align: 8
    .kernarg_segment_size: 48
    .language:       OpenCL C
    .language_version:
      - 2
      - 0
    .max_flat_workgroup_size: 512
    .name:           _Z11attn_kernelPKDF16_S0_S0_PfPDF16_S1_
    .private_segment_fixed_size: 0
    .sgpr_count:     82
    .sgpr_spill_count: 0
    .symbol:         _Z11attn_kernelPKDF16_S0_S0_PfPDF16_S1_.kd
    .uniform_work_group_size: 1
    .uses_dynamic_stack: false
    .vgpr_count:     120
    .vgpr_spill_count: 0
    .wavefront_size: 64
  - .agpr_count:     0
    .args:
      - .actual_access:  read_only
        .address_space:  global
        .offset:         0
        .size:           8
        .value_kind:     global_buffer
      - .actual_access:  read_only
        .address_space:  global
        .offset:         8
        .size:           8
        .value_kind:     global_buffer
      - .actual_access:  write_only
        .address_space:  global
        .offset:         16
        .size:           8
        .value_kind:     global_buffer
    .group_segment_fixed_size: 0
    .kernarg_segment_align: 8
    .kernarg_segment_size: 24
    .language:       OpenCL C
    .language_version:
      - 2
      - 0
    .max_flat_workgroup_size: 256
    .name:           _Z14combine_kernelPKDF16_PKfPf
    .private_segment_fixed_size: 0
    .sgpr_count:     70
    .sgpr_spill_count: 0
    .symbol:         _Z14combine_kernelPKDF16_PKfPf.kd
    .uniform_work_group_size: 1
    .uses_dynamic_stack: false
    .vgpr_count:     46
    .vgpr_spill_count: 0
    .wavefront_size: 64
